# hybrid with split at chunk 136 plus 2 weight-conversion blocks per wave moved into the idle P1 tail workgroups
# speedup vs baseline: 1.0415x; 1.0035x over previous
; #define LAS __attribute__((address_space(3)))
; __device__ __forceinline__ unsigned f2bf(float f) { return cvt_pk_bf16_nat(f, 0.f) & 0xffffu; }
; #define CONV_LD(ss_, buf_) { const int sc_ = (ss_) < nhalf ? (ss_) : nhalf - 1; const int fi_ = cw + (sc_ / NHB) * STRIDE, e_ = fi_ / FPE, r_ = fi_ % FPE; \
;                 if (r_ < F1) tr_load2(w1 + (size_t)e_ * D * 4096, 4096, r_, sc_ % NHB, lane, buf_); else tr_load2(w2 + (size_t)e_ * DFF * D, D, r_ - F1, sc_ % NHB, lane, buf_); }
; __global__ void __launch_bounds__(NTHR, 2) mk_fwd(Args args) {
;     ...
;         if (bx >= NWG / 2) {
;             LAS float* scr = (LAS float*)(lds + wave * 16640);
;             const int hw = (bx - NWG / 2) * NWAVES + wave; constexpr int HW = (NWG / 2) * NWAVES;
;             for (int it = hw; it < (D / 64) * (D / 64); it += HW) transpose_item(w_out, D, D, WOUTT, 0, scr, it, lane);
;         for (int i = hw * 64 + lane; i < 3072 * LK; i += HW * 64) {
;             const int n = i / LK, k = i % LK; float v = 0.f;
;             if (n < 1024) { if (k < 64) v = w2d[k * 1024 + n]; }
;             else if (n < 2048) { if (k >= 64 && k < 128) v = a2[(k - 64) * 1024 + (n - 1024)]; }
;             else { if (k >= 128 && k < 288) v = g2[(k - 128) * 1024 + (n - 2048)]; }
;             LORAT[i] = (bf16)f2bf(v);
;         }
;         for (int i = hw * 64 + lane; i < 1024 * 256; i += HW * 64) {
;             const int n = i >> 8, c = i & 255, g = n >> 8, d = n & 255;
;             WPOOLT[i] = (bf16)f2bf(w_pool[((size_t)g * 256 + c) * 256 + d]);
;         }
;         }
;     ...
;         else for (int crep_ = 0; crep_ < P5_CONV_REPS; ++crep_) {
;             LAS unsigned* img = (LAS unsigned*)(lds + wave * (4096 * NHB));
;             const int cw = (xcd_i * (32 - NSCAN_X) + slot_i - NSCAN_X) * NWAVES + wave;
;             constexpr int F1 = (D / (64 * NHB)) * (4096 / 64), F2 = (DFF / (64 * NHB)) * (D / 64), FPE = F1 + F2, NFULL = NE * FPE, STRIDE = (NWG - 8 * NSCAN_X) * NWAVES;
;             const int nhalf = cw < NFULL ? NHB * ((NFULL - cw + STRIDE - 1) / STRIDE) : 0;
;             f32x4 va[16], vb2[16], vc[16];
;             int s = 0;
;     ...
;             if (nhalf > 0) { CONV_LD(0, va); CONV_LD(1, vb2);
;                 for (;;) { CONV_STEP(va, vc); if (s >= nhalf) break; CONV_STEP(vb2, va); if (s >= nhalf) break; CONV_STEP(vc, vb2); if (s >= nhalf) break; } }
.LBB0_130:
	s_waitcnt lgkmcnt(0)
	s_barrier
	v_writelane_b32 v253, s2, 0
	v_writelane_b32 v253, s3, 1
	v_writelane_b32 v253, s4, 2
	v_writelane_b32 v253, s5, 3
	v_writelane_b32 v253, s6, 4
	v_writelane_b32 v253, s7, 5
	v_writelane_b32 v253, s8, 6
	v_writelane_b32 v253, s9, 7
	v_writelane_b32 v253, s10, 8
	v_writelane_b32 v253, s11, 9
	v_writelane_b32 v253, s12, 10
	v_writelane_b32 v253, s13, 11
	v_writelane_b32 v253, s14, 12
	v_writelane_b32 v253, s15, 13
	v_writelane_b32 v253, s16, 14
	v_writelane_b32 v253, s17, 15
	v_writelane_b32 v253, s29, 16
	v_writelane_b32 v253, s31, 17
	v_writelane_b32 v253, s34, 18
	v_writelane_b32 v253, s35, 19
	v_writelane_b32 v253, s36, 20
	v_writelane_b32 v253, s37, 21
	v_writelane_b32 v253, s38, 22
	v_writelane_b32 v253, s39, 23
	v_writelane_b32 v253, s40, 24
	v_writelane_b32 v253, s41, 25
	v_writelane_b32 v253, s42, 26
	v_writelane_b32 v253, s43, 27
	v_writelane_b32 v253, s44, 28
	v_writelane_b32 v253, s45, 29
	v_writelane_b32 v253, s46, 30
	v_writelane_b32 v253, s47, 31
	v_writelane_b32 v253, s48, 32
	v_writelane_b32 v253, s49, 33
	v_writelane_b32 v253, s50, 34
	v_writelane_b32 v253, s51, 35
	v_writelane_b32 v253, s52, 36
	v_writelane_b32 v253, s53, 37
	v_writelane_b32 v253, s54, 38
	v_writelane_b32 v253, s55, 39
	v_writelane_b32 v253, s72, 40
	v_writelane_b32 v253, vcc_lo, 41
	v_writelane_b32 v253, vcc_hi, 42
	s_lshl_b32 s3, s18, 3
	v_readlane_b32 s2, v252, 43
	s_nop 3
	s_add_i32 s3, s3, s2
	s_addk_i32 s3, 21504
	s_movk_i32 s2, 21055
	s_add_u32 s29, s26, 0x68c08000
	s_addc_u32 s72, s27, 0
	s_mov_b32 s98, 1
	s_movk_i32 s99, 0x400
	s_branch .Lconv_shared_entry
.Lconv_p1_return:
	v_readlane_b32 s2, v253, 0
	v_readlane_b32 s3, v253, 1
	v_readlane_b32 s4, v253, 2
	v_readlane_b32 s5, v253, 3
	v_readlane_b32 s6, v253, 4
	v_readlane_b32 s7, v253, 5
	v_readlane_b32 s8, v253, 6
	v_readlane_b32 s9, v253, 7
	v_readlane_b32 s10, v253, 8
	v_readlane_b32 s11, v253, 9
	v_readlane_b32 s12, v253, 10
	v_readlane_b32 s13, v253, 11
	v_readlane_b32 s14, v253, 12
	v_readlane_b32 s15, v253, 13
	v_readlane_b32 s16, v253, 14
	v_readlane_b32 s17, v253, 15
	v_readlane_b32 s29, v253, 16
	v_readlane_b32 s31, v253, 17
	v_readlane_b32 s34, v253, 18
	v_readlane_b32 s35, v253, 19
	v_readlane_b32 s36, v253, 20
	v_readlane_b32 s37, v253, 21
	v_readlane_b32 s38, v253, 22
	v_readlane_b32 s39, v253, 23
	v_readlane_b32 s40, v253, 24
	v_readlane_b32 s41, v253, 25
	v_readlane_b32 s42, v253, 26
	v_readlane_b32 s43, v253, 27
	v_readlane_b32 s44, v253, 28
	v_readlane_b32 s45, v253, 29
	v_readlane_b32 s46, v253, 30
	v_readlane_b32 s47, v253, 31
	v_readlane_b32 s48, v253, 32
	v_readlane_b32 s49, v253, 33
	v_readlane_b32 s50, v253, 34
	v_readlane_b32 s51, v253, 35
	v_readlane_b32 s52, v253, 36
	v_readlane_b32 s53, v253, 37
	v_readlane_b32 s54, v253, 38
	v_readlane_b32 s55, v253, 39
	v_readlane_b32 s72, v253, 40
	v_readlane_b32 vcc_lo, v253, 41
	v_readlane_b32 vcc_hi, v253, 42
	s_nop 3

; #define LAS __attribute__((address_space(3)))
; __global__ void __launch_bounds__(NTHR, 2) mk_fwd(Args args) {
;     ...
;                 const int j = lane;
;                 LAS bf16* IMG = (LAS bf16*)(lds + wave * 13312);
;                 LAS bf16* QGT = (LAS bf16*)(lds + wave * 13312 + 10240);
;                 for (int i = lane; i < 768; i += 64) ((LAS unsigned*)QGT)[i] = 0u;
;                 const int pos = (j & 32) | ((j & 12) << 1) | ((j & 16) >> 2) | (j & 3);
;                 bf16 nr_[17], nk_[17], nv_[17], nwl_[16], nal_[16]; float ncst_[7];
;     ...
;                 if (gw < 64 * NCHUNK) P4_FETCH(gw);
.LBB0_472:
	s_cmp_lt_i32 s88, 5
	s_cselect_b64 s[0:1], -1, 0
	s_and_b64 s[2:3], s[0:1], s[2:3]
	s_andn2_b64 vcc, exec, s[2:3]
	s_cbranch_vccnz .LBB0_481
	s_cmp_lt_i32 s18, 64
	s_cbranch_scc1 .LBB0_481
	v_writelane_b32 v252, s28, 54
	v_writelane_b32 v252, s30, 55
	v_readlane_b32 s0, v252, 38
	s_nop 3
	s_mul_i32 s0, s0, 24
	v_readlane_b32 s1, v252, 39
	s_nop 3
	s_add_i32 s0, s0, s1
	s_lshl_b32 s0, s0, 3
	v_readlane_b32 s1, v252, 43
	s_nop 3
	s_add_i32 s0, s1, s0
	s_sub_i32 s1, s0, 64
	s_and_b32 s0, s1, 63
	s_lshr_b32 s1, s1, 6
	s_add_i32 s1, s1, 136
	s_lshl_b32 s1, s1, 4
	s_lshr_b32 s30, s0, 4
	s_lshl_b32 s30, s30, 12
	s_add_i32 s101, s30, 0x1000
	s_and_b32 s0, s0, 15
	s_or_b32 s30, s30, s0
	s_or_b32 s30, s30, s1
	s_movk_i32 s28, 0x180
	v_readlane_b32 s0, v252, 43
	s_mulk_i32 s0, 0x3400
	s_add_i32 s4, s0, 0
	s_mov_b32 s77, 0
	s_cmpk_gt_i32 s30, 0x3fff
	v_lshl_add_u32 v125, v194, 2, s4
	v_mov_b32_e32 v7, 0
	ds_write2st64_b32 v125, v7, v7 offset0:40 offset1:41
	ds_write2st64_b32 v125, v7, v7 offset0:42 offset1:43
	ds_write2st64_b32 v125, v7, v7 offset0:44 offset1:45
	ds_write2st64_b32 v125, v7, v7 offset0:46 offset1:47
	ds_write2st64_b32 v125, v7, v7 offset0:48 offset1:49
	ds_write2st64_b32 v125, v7, v7 offset0:50 offset1:51
	s_cbranch_scc1 .LBB0_481
	v_writelane_b32 v252, s2, 52
	s_ashr_i32 s0, s30, 12
	s_lshl_b32 s5, s30, 6
	v_writelane_b32 v252, s3, 53
	s_bfe_u32 s2, s30, 0x80004
	s_ashr_i32 s1, s0, 31
	s_lshl_b32 s3, s2, 4
	s_and_b32 s5, s5, 0x3c0
	s_add_u32 s29, s26, 0x21c08000
	s_addc_u32 s31, s27, 0
	s_lshl_b32 s8, s5, 1
	s_add_u32 s6, s66, s8
	s_addc_u32 s7, s67, 0
	s_add_u32 s8, s10, s8
	s_addc_u32 s9, s11, 0
	s_lshl_b64 s[12:13], s[0:1], 12
	v_lshlrev_b32_e32 v1, 1, v0
	v_lshrrev_b32_e32 v2, 2, v0
	s_or_b32 s0, s12, s3
	v_and_b32_e32 v92, 15, v0
	v_and_b32_e32 v1, 24, v1
	v_and_b32_e32 v2, 4, v2
	v_and_b32_e32 v4, 3, v0
	v_and_b32_e32 v3, 35, v0
	s_add_u32 s1, s0, -1
	v_lshlrev_b32_e32 v5, 3, v0
	v_or3_b32 v101, v3, v2, v1
	s_addc_u32 s14, s13, -1
	v_and_b32_e32 v97, 56, v5
	v_mul_u32_u24_e32 v5, 0x48, v92
	v_lshlrev_b32_e32 v1, 1, v1
	v_lshlrev_b32_e32 v4, 1, v4
	s_cmp_eq_u32 s2, 0
	v_lshlrev_b32_e32 v5, 1, v5
	v_add3_u32 v1, s4, v1, v4
	v_lshlrev_b32_e32 v18, 1, v194
	v_mov_b32_e32 v19, v7
	v_and_b32_e32 v4, 48, v194
	v_lshl_add_u64 v[14:15], s[10:11], 0, v[18:19]
	v_lshl_add_u64 v[16:17], s[66:67], 0, v[18:19]
	v_add3_u32 v98, s4, v5, v4
	v_lshl_add_u64 v[4:5], s[6:7], 0, v[18:19]
	v_lshl_add_u64 v[18:19], s[8:9], 0, v[18:19]
	s_cselect_b32 s1, s12, s1
	s_cselect_b32 s6, s13, s14
	v_mov_b32_e32 v99, 0x2400
	s_mul_i32 s8, s6, 0x2400
	v_mad_u64_u32 v[22:23], s[6:7], s1, v99, v[18:19]
	v_add_u32_e32 v23, s8, v23
	s_movk_i32 s36, 0x1000
	global_load_ushort v24, v[22:23], off
	global_load_ushort v21, v[22:23], off offset:2048
	v_add_co_u32_e32 v22, vcc, s36, v22
	v_mad_i64_i32 v[18:19], s[6:7], s0, v99, v[18:19]
	s_nop 0
	v_addc_co_u32_e32 v23, vcc, 0, v23, vcc
	v_add_co_u32_e32 v26, vcc, s36, v18
	s_movk_i32 s37, 0x2000
	s_nop 0
	v_addc_co_u32_e32 v27, vcc, 0, v19, vcc
	global_load_ushort v20, v[22:23], off
	global_load_ushort v25, v[18:19], off
	s_nop 0
	global_load_ushort v22, v[18:19], off offset:2048
	global_load_ushort v23, v[26:27], off
	s_mov_b64 s[6:7], 0x2400
	v_add_co_u32_e32 v26, vcc, s37, v18
	v_lshl_add_u64 v[28:29], v[18:19], 0, s[6:7]
	s_nop 0
	v_addc_co_u32_e32 v27, vcc, 0, v19, vcc
	s_movk_i32 s38, 0x3000
	global_load_ushort v27, v[26:27], off offset:1024
	s_nop 0
	global_load_ushort v26, v[28:29], off offset:2048
	v_add_co_u32_e32 v28, vcc, s38, v18
	s_movk_i32 s8, 0x4000
	s_nop 0
	v_addc_co_u32_e32 v29, vcc, 0, v19, vcc
	global_load_ushort v96, v[28:29], off offset:1024
	v_add_co_u32_e32 v28, vcc, s8, v18
	s_movk_i32 s1, 0x5000
	s_nop 0
	v_addc_co_u32_e32 v29, vcc, 0, v19, vcc
	s_mov_b64 s[6:7], 0x4800
	v_add_co_u32_e32 v32, vcc, s1, v18
	v_lshl_add_u64 v[30:31], v[18:19], 0, s[6:7]
	s_nop 0
	v_addc_co_u32_e32 v33, vcc, 0, v19, vcc
	s_movk_i32 s9, 0x6000
	global_load_ushort v29, v[28:29], off offset:2048
	s_nop 0
	global_load_ushort v30, v[30:31], off offset:2048
	s_mov_b64 s[10:11], 0x6c00
	global_load_ushort v121, v[32:33], off offset:2048
	v_add_co_u32_e32 v32, vcc, s9, v18
	v_lshl_add_u64 v[34:35], v[18:19], 0, s[10:11]
	s_nop 0
	v_addc_co_u32_e32 v33, vcc, 0, v19, vcc
	s_movk_i32 s42, 0x7000
	global_load_ushort v32, v[32:33], off offset:3072
	s_nop 0
	global_load_ushort v31, v[34:35], off offset:2048
	v_add_co_u32_e32 v34, vcc, s42, v18
	s_mov_b32 s44, 0xa000
	s_nop 0
	v_addc_co_u32_e32 v35, vcc, 0, v19, vcc
	s_mov_b64 s[10:11], 0x9000
	v_add_co_u32_e32 v36, vcc, s44, v18
	global_load_ushort v122, v[34:35], off offset:3072
	v_lshl_add_u64 v[34:35], v[18:19], 0, s[10:11]
	v_addc_co_u32_e32 v37, vcc, 0, v19, vcc
	s_mov_b32 s1, 0xb000
	global_load_ushort v33, v[36:37], off offset:-4096
	s_nop 0
	global_load_ushort v34, v[34:35], off offset:2048
	s_nop 0
	global_load_ushort v123, v[36:37], off
	s_mov_b64 s[14:15], 0xb400
	v_add_co_u32_e32 v36, vcc, s1, v18
	v_lshl_add_u64 v[38:39], v[18:19], 0, s[14:15]
	s_nop 0
	v_addc_co_u32_e32 v37, vcc, 0, v19, vcc
	s_mov_b32 s39, 0xc000
	global_load_ushort v36, v[36:37], off offset:1024
	s_nop 0
	global_load_ushort v35, v[38:39], off offset:2048
	v_add_co_u32_e32 v38, vcc, s39, v18
	s_mov_b32 s41, 0xd000
	s_nop 0
	v_addc_co_u32_e32 v39, vcc, 0, v19, vcc
	global_load_ushort v124, v[38:39], off offset:1024
	s_mov_b64 s[14:15], 0xd800
	v_add_co_u32_e32 v38, vcc, s41, v18
	v_lshl_add_u64 v[40:41], v[18:19], 0, s[14:15]
	s_nop 0
	v_addc_co_u32_e32 v39, vcc, 0, v19, vcc
	s_mov_b32 s1, 0xe000
	global_load_ushort v38, v[38:39], off offset:2048
	s_nop 0
	global_load_ushort v37, v[40:41], off offset:2048
	v_add_co_u32_e32 v40, vcc, s1, v18
	s_mov_b32 s49, 0xf000
	s_nop 0
	v_addc_co_u32_e32 v41, vcc, 0, v19, vcc
	s_mov_b64 s[16:17], 0xfc00
	v_add_co_u32_e32 v42, vcc, s49, v18
	global_load_ushort v127, v[40:41], off offset:2048
	v_lshl_add_u64 v[40:41], v[18:19], 0, s[16:17]
	v_addc_co_u32_e32 v43, vcc, 0, v19, vcc
	s_mov_b32 s50, 0x10000
	global_load_ushort v43, v[42:43], off offset:3072
	s_nop 0
	global_load_ushort v39, v[40:41], off offset:2048
	v_add_co_u32_e32 v40, vcc, s50, v18
	s_mov_b32 s73, 0x13000
	s_nop 0
	v_addc_co_u32_e32 v41, vcc, 0, v19, vcc
	s_mov_b64 s[46:47], 0x12000
	v_add_co_u32_e32 v46, vcc, s73, v18
	global_load_ushort v128, v[40:41], off offset:3072
	v_lshl_add_u64 v[40:41], v[18:19], 0, s[46:47]
	v_addc_co_u32_e32 v47, vcc, 0, v19, vcc
	s_mov_b32 s1, 0x14000
	global_load_ushort v45, v[46:47], off offset:-4096
	global_load_ushort v44, v[40:41], off offset:2048
	s_nop 0
	global_load_ushort v41, v[46:47], off
	s_mov_b64 s[16:17], 0x14400
	v_add_co_u32_e32 v46, vcc, s1, v18
	v_lshl_add_u64 v[48:49], v[18:19], 0, s[16:17]
	s_nop 0
	v_addc_co_u32_e32 v47, vcc, 0, v19, vcc
	s_mov_b32 s78, 0x15000
	global_load_ushort v47, v[46:47], off offset:1024
	s_nop 0
	global_load_ushort v46, v[48:49], off offset:2048
	v_add_co_u32_e32 v48, vcc, s78, v18
	s_mov_b32 s72, 0x16000
	s_nop 0
	v_addc_co_u32_e32 v49, vcc, 0, v19, vcc
	global_load_ushort v129, v[48:49], off offset:1024
	s_mov_b64 s[16:17], 0x16800
	v_add_co_u32_e32 v48, vcc, s72, v18
	v_lshl_add_u64 v[50:51], v[18:19], 0, s[16:17]
	s_nop 0
	v_addc_co_u32_e32 v49, vcc, 0, v19, vcc
	s_mov_b32 s1, 0x17000
	global_load_ushort v49, v[48:49], off offset:2048
	s_nop 0
	global_load_ushort v48, v[50:51], off offset:2048
	v_add_co_u32_e32 v50, vcc, s1, v18
	s_mov_b32 s1, 0x18000
	s_nop 0
	v_addc_co_u32_e32 v51, vcc, 0, v19, vcc
	global_load_ushort v130, v[50:51], off offset:2048
	s_mov_b64 s[34:35], 0x18c00
	v_add_co_u32_e32 v50, vcc, s1, v18
	v_lshl_add_u64 v[52:53], v[18:19], 0, s[34:35]
	s_nop 0
	v_addc_co_u32_e32 v51, vcc, 0, v19, vcc
	s_mov_b32 s1, 0x19000
	global_load_ushort v51, v[50:51], off offset:3072
	s_nop 0
	global_load_ushort v50, v[52:53], off offset:2048
	v_add_co_u32_e32 v52, vcc, s1, v18
	s_mov_b32 s1, 0x1c000
	s_nop 0
	v_addc_co_u32_e32 v53, vcc, 0, v19, vcc
	s_mov_b64 s[34:35], 0x1b000
	v_add_co_u32_e32 v56, vcc, s1, v18
	v_lshl_add_u64 v[54:55], v[18:19], 0, s[34:35]
	s_nop 0
	v_addc_co_u32_e32 v57, vcc, 0, v19, vcc
	s_mov_b32 s1, 0x1d000
	global_load_ushort v133, v[52:53], off offset:3072
	s_nop 0
	global_load_ushort v53, v[56:57], off offset:-4096
	global_load_ushort v52, v[54:55], off offset:2048
	global_load_ushort v134, v[56:57], off
	s_mov_b64 s[34:35], 0x1d400
	v_add_co_u32_e32 v54, vcc, s1, v18
	v_lshl_add_u64 v[56:57], v[18:19], 0, s[34:35]
	s_nop 0
	v_addc_co_u32_e32 v55, vcc, 0, v19, vcc
	s_mov_b32 s1, 0x1e000
	global_load_ushort v55, v[54:55], off offset:1024
	s_nop 0
	global_load_ushort v54, v[56:57], off offset:2048
	v_add_co_u32_e32 v56, vcc, s1, v18
	s_mov_b32 s1, 0x1f000
	s_nop 0
	v_addc_co_u32_e32 v57, vcc, 0, v19, vcc
	v_add_co_u32_e32 v58, vcc, s1, v18
	s_mov_b32 s1, 0x20000
	s_nop 0
	v_addc_co_u32_e32 v59, vcc, 0, v19, vcc
	v_add_co_u32_e32 v60, vcc, s1, v18
	s_mov_b32 s1, 0x21000
	s_nop 0
	v_addc_co_u32_e32 v61, vcc, 0, v19, vcc
	s_mov_b64 s[34:35], 0x1f800
	v_add_co_u32_e32 v62, vcc, s1, v18
	global_load_ushort v135, v[56:57], off offset:1024
	v_lshl_add_u64 v[56:57], v[18:19], 0, s[34:35]
	s_mov_b64 s[34:35], 0x21c00
	v_addc_co_u32_e32 v63, vcc, 0, v19, vcc
	s_mov_b32 s1, 0x22000
	global_load_ushort v59, v[58:59], off offset:2048
	s_nop 0
	global_load_ushort v56, v[56:57], off offset:2048
	v_mov_b32_e32 v100, 0x1800
	global_load_ushort v136, v[60:61], off offset:2048
	v_lshl_add_u64 v[60:61], v[18:19], 0, s[34:35]
	v_add_co_u32_e32 v18, vcc, s1, v18
	v_mad_i64_i32 v[4:5], s[0:1], s0, v100, v[4:5]
	s_nop 0
	v_addc_co_u32_e32 v19, vcc, 0, v19, vcc
	global_load_ushort v64, v[62:63], off offset:3072
	s_nop 0
	global_load_ushort v61, v[60:61], off offset:2048
	v_add_co_u32_e32 v62, vcc, s36, v4
	s_mov_b64 s[0:1], 0x1800
	s_nop 0
	v_addc_co_u32_e32 v63, vcc, 0, v5, vcc
	v_add_co_u32_e32 v66, vcc, s38, v4
	global_load_ushort v137, v[18:19], off offset:3072
	v_lshl_add_u64 v[18:19], v[4:5], 0, s[0:1]
	s_mov_b64 s[0:1], 0x3000
	v_addc_co_u32_e32 v67, vcc, 0, v5, vcc
	global_load_ushort v58, v[4:5], off
	global_load_ushort v57, v[4:5], off offset:2048
	s_nop 0
	global_load_ushort v62, v[62:63], off offset:2048
	s_nop 0
	global_load_ushort v60, v[18:19], off offset:2048
	v_lshl_add_u64 v[18:19], v[4:5], 0, s[0:1]
	global_load_ushort v65, v[66:67], off
	global_load_ushort v63, v[18:19], off offset:2048
	v_add_co_u32_e32 v66, vcc, s8, v4
	s_mov_b32 s12, 0x9000
	s_nop 0
	v_addc_co_u32_e32 v67, vcc, 0, v5, vcc
	v_add_co_u32_e32 v68, vcc, s9, v4
	v_lshl_add_u64 v[18:19], v[4:5], 0, s[6:7]
	s_nop 0
	v_addc_co_u32_e32 v69, vcc, 0, v5, vcc
	v_add_co_u32_e32 v70, vcc, s42, v4
	s_mov_b64 s[0:1], 0x6000
	s_nop 0
	v_addc_co_u32_e32 v71, vcc, 0, v5, vcc
	v_add_co_u32_e32 v72, vcc, s12, v4
	global_load_ushort v67, v[66:67], off offset:2048
	s_nop 0
	global_load_ushort v66, v[18:19], off offset:2048
	v_addc_co_u32_e32 v73, vcc, 0, v5, vcc
	v_add_co_u32_e32 v74, vcc, s44, v4
	v_lshl_add_u64 v[18:19], v[4:5], 0, s[0:1]
	s_nop 0
	v_addc_co_u32_e32 v75, vcc, 0, v5, vcc
	v_add_co_u32_e32 v76, vcc, s39, v4
	s_mov_b64 s[0:1], 0x7800
	s_nop 0
	v_addc_co_u32_e32 v77, vcc, 0, v5, vcc
	v_add_co_u32_e32 v78, vcc, s41, v4
	global_load_ushort v69, v[68:69], off
	s_nop 0
	global_load_ushort v68, v[18:19], off offset:2048
	v_addc_co_u32_e32 v79, vcc, 0, v5, vcc
; __device__ __forceinline__ unsigned f2bf(float f) { return cvt_pk_bf16_nat(f, 0.f) & 0xffffu; }
; __global__ void __launch_bounds__(NTHR, 2) mk_fwd(Args args) {
;     ...
;                 if (gw < 64 * NCHUNK) P4_FETCH(gw);
;     ...
;                     const int s_ = tr, rec = (s_ >> 2) * 8 + (s_ & 3);
; #pragma unroll
;                     for (int e = 0; e < 4; ++e) { const int t = 4 * q + e;
;                         const float qv = s_ < t ? QT[e] : 0.f, gb = s_ <= t ? GB[e] : 0.f, gk = s_ <= t ? GK[e] : 0.f;
;                         QGT[t * 32 + rec] = (bf16)f2bf(qv);
;                         QGT[512 + t * 32 + rec] = (bf16)f2bf(gb); QGT[512 + t * 32 + rec + 4] = (bf16)f2bf(gk); }
;                     float Tr[16]; const pg8::v4i_t PTi = __builtin_bit_cast(pg8::v4i_t, PT);
; #pragma unroll
;                     for (int t = 0; t < 16; ++t) { float acc = (t == s_) ? 1.f : 0.f;
	v_lshl_add_u64 v[18:19], v[4:5], 0, s[0:1]
	v_add_co_u32_e32 v80, vcc, s49, v4
	global_load_ushort v71, v[70:71], off offset:2048
	s_nop 0
	global_load_ushort v70, v[18:19], off offset:2048
	v_lshl_add_u64 v[18:19], v[4:5], 0, s[10:11]
	s_mov_b64 s[0:1], 0xa800
	v_addc_co_u32_e32 v81, vcc, 0, v5, vcc
	global_load_ushort v73, v[72:73], off
	s_nop 0
	global_load_ushort v72, v[18:19], off offset:2048
	v_lshl_add_u64 v[18:19], v[4:5], 0, s[0:1]
	s_mov_b64 s[0:1], 0xc000
	v_add_co_u32_e32 v82, vcc, s50, v4
	s_mov_b32 s13, 0x12000
	global_load_ushort v75, v[74:75], off offset:2048
	s_nop 0
	global_load_ushort v74, v[18:19], off offset:2048
	v_lshl_add_u64 v[18:19], v[4:5], 0, s[0:1]
	v_addc_co_u32_e32 v83, vcc, 0, v5, vcc
	global_load_ushort v77, v[76:77], off
	s_nop 0
	global_load_ushort v76, v[18:19], off offset:2048
	v_lshl_add_u64 v[18:19], v[4:5], 0, s[14:15]
	s_mov_b64 s[0:1], 0xf000
	v_add_co_u32_e32 v84, vcc, s13, v4
	global_load_ushort v79, v[78:79], off offset:2048
	s_nop 0
	global_load_ushort v78, v[18:19], off offset:2048
	v_lshl_add_u64 v[18:19], v[4:5], 0, s[0:1]
	s_mov_b64 s[0:1], 0x10800
	v_addc_co_u32_e32 v85, vcc, 0, v5, vcc
	global_load_ushort v81, v[80:81], off
	s_nop 0
	global_load_ushort v80, v[18:19], off offset:2048
	v_lshl_add_u64 v[18:19], v[4:5], 0, s[0:1]
	v_add_co_u32_e32 v86, vcc, s73, v4
	global_load_ushort v83, v[82:83], off offset:2048
	s_nop 0
	global_load_ushort v82, v[18:19], off offset:2048
	v_lshl_add_u64 v[18:19], v[4:5], 0, s[46:47]
	s_mov_b64 s[0:1], 0x13800
	v_addc_co_u32_e32 v87, vcc, 0, v5, vcc
	global_load_ushort v85, v[84:85], off
	s_nop 0
	global_load_ushort v84, v[18:19], off offset:2048
	v_lshl_add_u64 v[18:19], v[4:5], 0, s[0:1]
	s_mov_b64 s[0:1], 0x15000
	v_add_co_u32_e32 v88, vcc, s78, v4
	v_or_b32_e32 v2, s5, v194
	v_readlane_b32 s80, v252, 0
	global_load_ushort v87, v[86:87], off offset:2048
	s_nop 0
	global_load_ushort v86, v[18:19], off offset:2048
	v_lshl_add_u64 v[18:19], v[4:5], 0, s[0:1]
	v_addc_co_u32_e32 v89, vcc, 0, v5, vcc
	v_lshlrev_b32_e32 v6, 2, v2
	v_readlane_b32 s84, v252, 4
	v_readlane_b32 s85, v252, 5
	global_load_ushort v89, v[88:89], off
	s_nop 0
	global_load_ushort v88, v[18:19], off offset:2048
	v_lshl_add_u64 v[18:19], v[4:5], 0, s[16:17]
	v_add_co_u32_e32 v4, vcc, s72, v4
	v_lshl_add_u64 v[2:3], s[84:85], 0, v[6:7]
	s_nop 0
	v_addc_co_u32_e32 v5, vcc, 0, v5, vcc
	v_add_co_u32_e32 v2, vcc, s37, v2
	v_readlane_b32 s86, v252, 6
	s_nop 0
	v_addc_co_u32_e32 v3, vcc, 0, v3, vcc
	v_readlane_b32 s87, v252, 7
	v_readlane_b32 s90, v252, 10
	v_readlane_b32 s91, v252, 11
	global_load_ushort v91, v[4:5], off offset:2048
	global_load_ushort v90, v[18:19], off offset:2048
	global_load_dword v40, v6, s[84:85]
	global_load_dword v42, v[2:3], off offset:-4096
	s_nop 0
	global_load_dword v2, v[2:3], off
	s_nop 0
	global_load_dword v95, v6, s[86:87]
	global_load_dword v94, v6, s[90:91]
	global_load_dword v28, v6, s[52:53]
	global_load_dword v3, v6, s[54:55]
	s_movk_i32 s5, 0x48
	v_lshrrev_b32_e32 v4, 3, v194
	v_mad_u32_u24 v4, v4, s5, v97
	v_lshrrev_b32_e32 v93, 4, v194
	v_lshl_add_u32 v102, v4, 1, s4
	v_or_b32_e32 v4, 64, v194
	v_lshlrev_b32_e32 v104, 2, v93
	v_lshrrev_b32_e32 v5, 3, v4
	v_mad_u32_u24 v5, v5, s5, v97
	v_or_b32_e32 v6, 2, v104
	v_cmp_eq_u32_e32 vcc, 0, v92
	v_lshl_add_u32 v101, v101, 1, s4
	v_lshl_add_u32 v103, v5, 1, s4
	v_cmp_lt_u32_e64 s[4:5], v92, v104
	v_cmp_gt_u32_e64 s[6:7], v92, v104
	v_or_b32_e32 v5, 1, v104
	v_cmp_lt_u32_e64 s[10:11], v92, v6
	v_cmp_gt_u32_e64 s[12:13], v92, v6
	v_lshlrev_b32_e32 v131, 6, v6
	v_or_b32_e32 v6, 3, v104
	v_cndmask_b32_e64 v104, 0, 1.0, vcc
	v_cmp_eq_u32_e32 vcc, 1, v92
	v_cvt_pk_bf16_f32 v120, v104, s0
	v_readlane_b32 s0, v252, 40
	v_cndmask_b32_e64 v105, 0, 1.0, vcc
	v_cmp_eq_u32_e32 vcc, 2, v92
	s_lshl_b32 s0, s0, 3
	v_readlane_b32 s1, v252, 43
	v_cndmask_b32_e64 v106, 0, 1.0, vcc
	v_cmp_eq_u32_e32 vcc, 3, v92
	s_add_i32 s0, s1, s0
	s_mov_b32 s45, 0x5040100
	v_cndmask_b32_e64 v107, 0, 1.0, vcc
	v_cmp_eq_u32_e32 vcc, 4, v92
	s_add_i32 s34, s0, s28
	v_readlane_b32 s0, v252, 37
	v_cndmask_b32_e64 v108, 0, 1.0, vcc
	v_cmp_eq_u32_e32 vcc, 5, v92
	v_mul_u32_u24_e32 v126, 12, v194
	v_lshlrev_b32_e32 v18, 4, v4
	v_cndmask_b32_e64 v109, 0, 1.0, vcc
	v_cmp_eq_u32_e32 vcc, 6, v92
	v_lshlrev_b32_e32 v4, 8, v93
	v_cmp_gt_u32_e64 s[8:9], v92, v5
	v_cndmask_b32_e64 v110, 0, 1.0, vcc
	v_cmp_eq_u32_e32 vcc, 7, v92
	v_lshlrev_b32_e32 v5, 6, v5
	v_cmp_lt_u32_e64 s[14:15], v92, v6
	v_cndmask_b32_e64 v111, 0, 1.0, vcc
	v_cmp_eq_u32_e32 vcc, 8, v92
	v_cmp_gt_u32_e64 s[16:17], v92, v6
	v_lshlrev_b32_e32 v132, 6, v6
	v_cndmask_b32_e64 v112, 0, 1.0, vcc
	v_cmp_eq_u32_e32 vcc, 9, v92
	s_waitcnt vmcnt(0)
; __global__ void __launch_bounds__(NTHR, 2) mk_fwd(Args args) {
;     ...
;                 if (gw < 64 * NCHUNK) P4_FETCH(gw);
; #pragma unroll 1
;                 for (int u = gw; u < 64 * NCHUNK; u += NGW) {
;                     const int h = u & 15, c = (u >> 4) & 255, b = u >> 12, hd = b * 16 + h;
;                     const float mu_r = ncst_[0], mu_k = ncst_[1], mu_v = ncst_[2], c_w0 = ncst_[3], c_a0 = ncst_[4], c_kk = ncst_[5], c_ka = ncst_[6];
;                     unsigned char* pk = ws + WS_R + ((size_t)hd * NCHUNK + c) * PK_BYTES;
;                     float At[16], Rt[16], Bt[16], Kt[16], Vt[16];
;                     float xr_[17], xk_[17], xv_[17], xwl_[16], xal_[16];
; #pragma unroll
;                     for (int t = 0; t < 17; ++t) { xr_[t] = __builtin_bit_cast(float, (unsigned)nr_[t] << 16); xk_[t] = __builtin_bit_cast(float, (unsigned)nk_[t] << 16); xv_[t] = __builtin_bit_cast(float, (unsigned)nv_[t] << 16); }
; #pragma unroll
;                     for (int t = 0; t < 16; ++t) { xwl_[t] = __builtin_bit_cast(float, (unsigned)nwl_[t] << 16); xal_[t] = __builtin_bit_cast(float, (unsigned)nal_[t] << 16); }
;                     if (c == 0) { xr_[0] = 0.f; xk_[0] = 0.f; xv_[0] = 0.f; }
	v_perm_b32 v212, v127, v124, s45
	v_perm_b32 v213, v128, v127, s45
	v_cndmask_b32_e64 v113, 0, 1.0, vcc
	v_cmp_eq_u32_e32 vcc, 10, v92
	v_perm_b32 v214, v123, v122, s45
	v_perm_b32 v215, v121, v96, s45
	v_cndmask_b32_e64 v114, 0, 1.0, vcc
	v_cmp_eq_u32_e32 vcc, 11, v92
	v_perm_b32 v93, v137, v136, s45
	v_perm_b32 v96, v134, v133, s45
	v_cndmask_b32_e64 v115, 0, 1.0, vcc
	v_cmp_eq_u32_e32 vcc, 12, v92
	v_perm_b32 v97, v130, v129, s45
	s_add_i32 s34, s30, s28
	v_cndmask_b32_e64 v116, 0, 1.0, vcc
	v_cmp_eq_u32_e32 vcc, 13, v92
	v_lshlrev_b32_e32 v8, 6, v194
	v_lshlrev_b32_e32 v10, 5, v194
	v_cndmask_b32_e64 v117, 0, 1.0, vcc
	v_cmp_eq_u32_e32 vcc, 14, v92
	v_mov_b32_e32 v11, v7
	v_cmp_gt_u32_e64 s[2:3], 16, v194
	v_cndmask_b32_e64 v118, 0, 1.0, vcc
	v_cmp_eq_u32_e32 vcc, 15, v92
	v_perm_b32 v92, v136, v135, s45
	v_lshlrev_b32_e32 v12, 4, v194
	v_mov_b32_e32 v9, v7
	v_mov_b32_e32 v13, v7
	v_mov_b32_e32 v19, v7
	v_cndmask_b32_e64 v119, 0, 1.0, vcc
	s_lshl_b32 s48, s34, 6
	s_lshl_b32 s51, s28, 6
	s_mov_b32 s79, 0xbfb8aa3b
	v_lshlrev_b32_e32 v6, 2, v194
	v_add_u32_e32 v121, v1, v4
	v_add_u32_e32 v122, v1, v5
	v_add_u32_e32 v123, v1, v131
	v_add_u32_e32 v124, v1, v132
	v_add_u32_e32 v125, v125, v126
	s_mov_b32 s34, s30
	v_mov_b32_e32 v160, v57
	v_mov_b32_e32 v163, v60
	v_mov_b32_e32 v166, v63
	v_mov_b32_e32 v169, v66
	v_mov_b32_e32 v171, v68
	v_mov_b32_e32 v173, v70
	v_mov_b32_e32 v175, v72
	v_mov_b32_e32 v177, v74
	v_mov_b32_e32 v179, v76
	v_mov_b32_e32 v181, v78
	v_mov_b32_e32 v183, v80
	v_mov_b32_e32 v185, v82
	v_mov_b32_e32 v187, v84
	v_mov_b32_e32 v189, v86
	v_mov_b32_e32 v191, v88
	v_mov_b32_e32 v193, v90
	v_mov_b32_e32 v162, v58
	v_mov_b32_e32 v165, v62
	v_mov_b32_e32 v168, v65
	v_mov_b32_e32 v170, v67
	v_mov_b32_e32 v172, v69
	v_mov_b32_e32 v174, v71
	v_mov_b32_e32 v176, v73
	v_mov_b32_e32 v178, v75
	v_mov_b32_e32 v180, v77
	v_mov_b32_e32 v182, v79
	v_mov_b32_e32 v184, v81
	v_mov_b32_e32 v186, v83
	v_mov_b32_e32 v188, v85
	v_mov_b32_e32 v190, v87
	v_mov_b32_e32 v192, v89
	v_mov_b32_e32 v196, v91
	v_mov_b32_e32 v127, v20
	v_mov_b32_e32 v130, v23
	v_mov_b32_e32 v146, v41
	v_mov_b32_e32 v126, v21
	v_mov_b32_e32 v129, v22
	v_mov_b32_e32 v132, v26
	v_mov_b32_e32 v134, v30
	v_mov_b32_e32 v136, v31
	v_mov_b32_e32 v138, v34
	v_mov_b32_e32 v140, v35
	v_mov_b32_e32 v142, v37
	v_mov_b32_e32 v144, v39
	v_mov_b32_e32 v147, v44
	v_mov_b32_e32 v149, v46
	v_mov_b32_e32 v151, v48
	v_mov_b32_e32 v153, v50
	v_mov_b32_e32 v155, v52
	v_mov_b32_e32 v157, v54
	v_mov_b32_e32 v159, v56
	v_mov_b32_e32 v164, v61
	v_mov_b32_e32 v128, v24
	v_mov_b32_e32 v131, v25
	v_mov_b32_e32 v133, v27
	v_mov_b32_e32 v135, v29
	v_mov_b32_e32 v137, v32
	v_mov_b32_e32 v139, v33
	v_mov_b32_e32 v141, v36
	v_mov_b32_e32 v143, v38
	v_mov_b32_e32 v145, v43
	v_mov_b32_e32 v148, v45
	v_mov_b32_e32 v150, v47
	v_mov_b32_e32 v152, v49
	v_mov_b32_e32 v154, v51
	v_mov_b32_e32 v156, v53
	v_mov_b32_e32 v158, v55
	v_mov_b32_e32 v161, v59
	v_mov_b32_e32 v167, v64
	v_mov_b32_e32 v197, v40
	v_mov_b32_e32 v198, v42
	v_mov_b32_e32 v200, v95
	v_mov_b32_e32 v201, v94
	v_mov_b32_e32 v202, v28
	v_mov_b32_e32 v203, v3
	v_mov_b32_e32 v204, v212
	v_mov_b32_e32 v205, v213
	v_mov_b32_e32 v206, v214
	v_mov_b32_e32 v207, v215
	v_mov_b32_e32 v208, v92
	v_mov_b32_e32 v209, v93
	v_mov_b32_e32 v210, v96
	v_mov_b32_e32 v211, v97
	v_readlane_b32 s81, v252, 1
	v_readlane_b32 s82, v252, 2
	v_readlane_b32 s83, v252, 3
	v_readlane_b32 s88, v252, 8
	v_readlane_b32 s89, v252, 9
	v_readlane_b32 s92, v252, 12
	v_readlane_b32 s93, v252, 13
	v_readlane_b32 s94, v252, 14
	v_readlane_b32 s95, v252, 15
	s_branch .LBB0_476

; #define LAS __attribute__((address_space(3)))
; __global__ void __launch_bounds__(NTHR, 2) mk_fwd(Args args) {
;     ...
;             LAS unsigned* img = (LAS unsigned*)(lds + wave * (4096 * NHB));
;             const int cw = (xcd_i * (32 - NSCAN_X) + slot_i - NSCAN_X) * NWAVES + wave;
;             constexpr int F1 = (D / (64 * NHB)) * (4096 / 64), F2 = (DFF / (64 * NHB)) * (D / 64), FPE = F1 + F2, NFULL = NE * FPE, STRIDE = (NWG - 8 * NSCAN_X) * NWAVES;
;             const int nhalf = cw < NFULL ? NHB * ((NFULL - cw + STRIDE - 1) / STRIDE) : 0;
;             f32x4 va[16], vb2[16], vc[16];
;             int s = 0;
.LBB0_535:
	s_cmp_lt_i32 s88, 6
	s_cselect_b64 s[2:3], -1, 0
	s_add_u32 s29, s26, 0x68c08000
	s_addc_u32 s72, s27, 0
	s_and_b64 s[0:1], s[2:3], s[0:1]
	s_andn2_b64 vcc, exec, s[0:1]
	s_cbranch_vccnz .LBB0_670
	s_cmp_lt_i32 s18, 64
	s_mov_b64 s[2:3], -1
	s_cbranch_scc1 .LBB0_586
	v_readlane_b32 s2, v252, 38
	s_mul_i32 s2, s2, 24
	v_readlane_b32 s3, v252, 39
	s_add_i32 s2, s2, s3
	s_lshl_b32 s2, s2, 3
	v_readlane_b32 s3, v252, 43
	s_add_i32 s2, s3, s2
	s_sub_i32 s3, s2, 64
	s_mov_b32 s98, 0
	s_movk_i32 s99, 0x600
.Lconv_shared_entry:
	s_cmpk_lt_i32 s3, 0x6000
	s_cselect_b64 s[4:5], -1, 0
	s_sub_i32 s2, 24127, s2
	s_cmpk_gt_u32 s2, 0x5ff
	s_cselect_b64 s[6:7], -1, 0
	s_and_b64 s[4:5], s[4:5], s[6:7]
	s_and_b64 vcc, exec, s[4:5]
	s_cbranch_vccz .LBB0_585
	s_mul_hi_i32 s4, s3, 0x2aaaaaab
	s_lshr_b32 s5, s4, 31
	s_ashr_i32 s4, s4, 7
	s_add_i32 s4, s4, s5
	s_mul_i32 s5, s4, 0x300
	s_sub_i32 s8, s3, s5
	s_ashr_i32 s5, s4, 31
	v_readlane_b32 s36, v252, 16
	s_lshl_b64 s[6:7], s[4:5], 24
	v_readlane_b32 s48, v252, 28
	v_readlane_b32 s49, v252, 29
	s_add_u32 s6, s48, s6
	s_addc_u32 s7, s49, s7
	s_lshl_b32 s9, s8, 3
	v_lshrrev_b32_e32 v1, 2, v0
	s_and_b32 s9, s9, 0x700
	v_and_b32_e32 v1, 12, v1
	v_or_b32_e32 v4, s9, v1
	s_lshl_b32 s9, s8, 8
	s_and_b32 s9, s9, 0x1f00
	v_and_b32_e32 v2, 60, v195
	s_add_u32 s6, s6, s9
	v_readlane_b32 s44, v252, 24
	s_addc_u32 s7, s7, 0
	v_mov_b32_e32 v197, 0
	v_lshlrev_b32_e32 v196, 2, v2
	s_lshl_b64 s[4:5], s[4:5], 25
	v_readlane_b32 s45, v252, 25
	v_lshl_add_u64 v[2:3], s[6:7], 0, v[196:197]
	s_add_u32 s6, s44, s4
	s_addc_u32 s7, s45, s5
	s_bfe_u32 s4, s8, 0x60019
	s_add_i32 s4, s8, s4
	s_sext_i32_i16 s9, s4
	s_and_b32 s4, s4, 0xffc0
	s_sub_i32 s4, s8, s4
	s_sext_i32_i16 s4, s4
	s_lshl_b32 s4, s4, 6
	s_ashr_i32 s5, s4, 31
	s_lshl_b64 s[4:5], s[4:5], 2
	s_add_u32 s4, s6, s4
	s_addc_u32 s5, s7, s5
	v_lshl_add_u64 v[66:67], s[4:5], 0, v[196:197]
	s_lshl_b32 s4, s9, 2
	v_lshlrev_b32_e32 v4, 13, v4
	v_mov_b32_e32 v5, v197
	s_and_b32 s4, s4, 0xffffff00
	v_lshl_add_u64 v[70:71], v[2:3], 0, v[4:5]
	v_or_b32_e32 v68, s4, v1
	s_mov_b64 s[4:5], 0x66000
	v_lshl_add_u64 v[34:35], v[70:71], 0, s[4:5]
	s_mov_b64 s[4:5], 0x64000
	v_lshl_add_u64 v[36:37], v[70:71], 0, s[4:5]
	s_mov_b64 s[4:5], 0x62000
	v_lshl_add_u64 v[38:39], v[70:71], 0, s[4:5]
	s_mov_b64 s[4:5], 0x60000
	v_lshl_add_u64 v[40:41], v[70:71], 0, s[4:5]
	s_mov_b64 s[4:5], 0x46000
	v_lshl_add_u64 v[42:43], v[70:71], 0, s[4:5]
	s_mov_b64 s[4:5], 0x44000
	v_lshl_add_u64 v[44:45], v[70:71], 0, s[4:5]
	s_mov_b64 s[4:5], 0x42000
	v_lshl_add_u64 v[46:47], v[70:71], 0, s[4:5]
	s_mov_b64 s[4:5], 0x40000
	v_lshl_add_u64 v[48:49], v[70:71], 0, s[4:5]
	s_mov_b64 s[4:5], 0x26000
	v_lshl_add_u64 v[50:51], v[70:71], 0, s[4:5]
	s_mov_b64 s[4:5], 0x24000
	v_lshl_add_u64 v[52:53], v[70:71], 0, s[4:5]
	s_mov_b64 s[4:5], 0x22000
	v_lshl_add_u64 v[54:55], v[70:71], 0, s[4:5]
	s_mov_b64 s[4:5], 0x20000
	v_or_b32_e32 v2, 51, v68
	v_or_b32_e32 v4, 50, v68
	v_or_b32_e32 v6, 49, v68
	v_or_b32_e32 v8, 48, v68
	v_or_b32_e32 v10, 35, v68
	v_or_b32_e32 v12, 34, v68
	v_or_b32_e32 v14, 33, v68
	v_or_b32_e32 v16, 32, v68
	v_or_b32_e32 v18, 19, v68
	v_or_b32_e32 v20, 18, v68
	v_or_b32_e32 v22, 17, v68
	v_or_b32_e32 v24, 16, v68
	v_or_b32_e32 v26, 3, v68
	v_or_b32_e32 v28, 2, v68
	v_or_b32_e32 v30, 1, v68
	v_lshl_add_u64 v[56:57], v[70:71], 0, s[4:5]
	s_mov_b64 s[4:5], 0x6000
	v_ashrrev_i32_e32 v3, 31, v2
	v_ashrrev_i32_e32 v5, 31, v4
	v_ashrrev_i32_e32 v7, 31, v6
	v_ashrrev_i32_e32 v9, 31, v8
	v_ashrrev_i32_e32 v11, 31, v10
	v_ashrrev_i32_e32 v13, 31, v12
	v_ashrrev_i32_e32 v15, 31, v14
	v_ashrrev_i32_e32 v17, 31, v16
	v_ashrrev_i32_e32 v19, 31, v18
	v_ashrrev_i32_e32 v21, 31, v20
	v_ashrrev_i32_e32 v23, 31, v22
	v_ashrrev_i32_e32 v25, 31, v24
	v_ashrrev_i32_e32 v27, 31, v26
	v_ashrrev_i32_e32 v29, 31, v28
	v_ashrrev_i32_e32 v31, 31, v30
	v_ashrrev_i32_e32 v69, 31, v68
	v_lshl_add_u64 v[58:59], v[70:71], 0, s[4:5]
	s_mov_b64 s[4:5], 0x4000
	v_lshlrev_b64 v[2:3], 14, v[2:3]
	v_lshlrev_b64 v[4:5], 14, v[4:5]
	v_lshlrev_b64 v[6:7], 14, v[6:7]
	v_lshlrev_b64 v[8:9], 14, v[8:9]
	v_lshlrev_b64 v[10:11], 14, v[10:11]
	v_lshlrev_b64 v[12:13], 14, v[12:13]
	v_lshlrev_b64 v[14:15], 14, v[14:15]
	v_lshlrev_b64 v[16:17], 14, v[16:17]
	v_lshlrev_b64 v[18:19], 14, v[18:19]
	v_lshlrev_b64 v[20:21], 14, v[20:21]
	v_lshlrev_b64 v[22:23], 14, v[22:23]
	v_lshlrev_b64 v[24:25], 14, v[24:25]
	v_lshlrev_b64 v[26:27], 14, v[26:27]
	v_lshlrev_b64 v[28:29], 14, v[28:29]
	v_lshlrev_b64 v[30:31], 14, v[30:31]
	v_lshlrev_b64 v[32:33], 14, v[68:69]
	v_lshl_add_u64 v[60:61], v[70:71], 0, s[4:5]
; #define CONV_LD(ss_, buf_) { const int sc_ = (ss_) < nhalf ? (ss_) : nhalf - 1; const int fi_ = cw + (sc_ / NHB) * STRIDE, e_ = fi_ / FPE, r_ = fi_ % FPE; \
;                 if (r_ < F1) tr_load2(w1 + (size_t)e_ * D * 4096, 4096, r_, sc_ % NHB, lane, buf_); else tr_load2(w2 + (size_t)e_ * DFF * D, D, r_ - F1, sc_ % NHB, lane, buf_); }
; __global__ void __launch_bounds__(NTHR, 2) mk_fwd(Args args) {
;     ...
;             if (nhalf > 0) { CONV_LD(0, va); CONV_LD(1, vb2);
;                 for (;;) { CONV_STEP(va, vc); if (s >= nhalf) break; CONV_STEP(vb2, va); if (s >= nhalf) break; CONV_STEP(vc, vb2); if (s >= nhalf) break; } }
	s_mov_b64 s[4:5], 0x2000
	s_cmpk_lt_i32 s8, 0x200
	v_lshl_add_u64 v[2:3], v[66:67], 0, v[2:3]
	v_lshl_add_u64 v[4:5], v[66:67], 0, v[4:5]
	v_lshl_add_u64 v[6:7], v[66:67], 0, v[6:7]
	v_lshl_add_u64 v[8:9], v[66:67], 0, v[8:9]
	v_lshl_add_u64 v[10:11], v[66:67], 0, v[10:11]
	v_lshl_add_u64 v[12:13], v[66:67], 0, v[12:13]
	v_lshl_add_u64 v[14:15], v[66:67], 0, v[14:15]
	v_lshl_add_u64 v[16:17], v[66:67], 0, v[16:17]
	v_lshl_add_u64 v[18:19], v[66:67], 0, v[18:19]
	v_lshl_add_u64 v[20:21], v[66:67], 0, v[20:21]
	v_lshl_add_u64 v[22:23], v[66:67], 0, v[22:23]
	v_lshl_add_u64 v[24:25], v[66:67], 0, v[24:25]
	v_lshl_add_u64 v[26:27], v[66:67], 0, v[26:27]
	v_lshl_add_u64 v[28:29], v[66:67], 0, v[28:29]
	v_lshl_add_u64 v[30:31], v[66:67], 0, v[30:31]
	v_lshl_add_u64 v[32:33], v[66:67], 0, v[32:33]
	v_lshl_add_u64 v[62:63], v[70:71], 0, s[4:5]
	s_cselect_b64 vcc, -1, 0
	v_cndmask_b32_e32 v65, v71, v33, vcc
	v_cndmask_b32_e32 v64, v70, v32, vcc
	v_cndmask_b32_e32 v63, v63, v31, vcc
	v_cndmask_b32_e32 v62, v62, v30, vcc
	v_cndmask_b32_e32 v61, v61, v29, vcc
	v_cndmask_b32_e32 v60, v60, v28, vcc
	v_cndmask_b32_e32 v59, v59, v27, vcc
	v_cndmask_b32_e32 v58, v58, v26, vcc
	v_cndmask_b32_e32 v57, v57, v25, vcc
	v_cndmask_b32_e32 v56, v56, v24, vcc
	v_cndmask_b32_e32 v55, v55, v23, vcc
	v_cndmask_b32_e32 v54, v54, v22, vcc
	v_cndmask_b32_e32 v53, v53, v21, vcc
	v_cndmask_b32_e32 v52, v52, v20, vcc
	v_cndmask_b32_e32 v51, v51, v19, vcc
	v_cndmask_b32_e32 v50, v50, v18, vcc
	v_cndmask_b32_e32 v31, v49, v17, vcc
	v_cndmask_b32_e32 v30, v48, v16, vcc
	v_cndmask_b32_e32 v27, v47, v15, vcc
	v_cndmask_b32_e32 v26, v46, v14, vcc
	v_cndmask_b32_e32 v23, v45, v13, vcc
	v_cndmask_b32_e32 v22, v44, v12, vcc
	v_cndmask_b32_e32 v19, v43, v11, vcc
	v_cndmask_b32_e32 v18, v42, v10, vcc
	v_cndmask_b32_e32 v15, v41, v9, vcc
	v_cndmask_b32_e32 v14, v40, v8, vcc
	v_cndmask_b32_e32 v11, v39, v7, vcc
	v_cndmask_b32_e32 v10, v38, v6, vcc
	v_cndmask_b32_e32 v7, v37, v5, vcc
	v_cndmask_b32_e32 v6, v36, v4, vcc
	v_cndmask_b32_e32 v3, v35, v3, vcc
	v_cndmask_b32_e32 v2, v34, v2, vcc
	global_load_dwordx4 v[2:5], v[2:3], off nt
	s_nop 0
	global_load_dwordx4 v[6:9], v[6:7], off nt
	s_nop 0
	global_load_dwordx4 v[10:13], v[10:11], off nt
	s_nop 0
	global_load_dwordx4 v[14:17], v[14:15], off nt
	s_nop 0
	global_load_dwordx4 v[18:21], v[18:19], off nt
	s_nop 0
	global_load_dwordx4 v[22:25], v[22:23], off nt
	s_nop 0
	global_load_dwordx4 v[26:29], v[26:27], off nt
	s_nop 0
	global_load_dwordx4 v[30:33], v[30:31], off nt
	s_nop 0
	global_load_dwordx4 v[34:37], v[50:51], off nt
	global_load_dwordx4 v[38:41], v[52:53], off nt
	global_load_dwordx4 v[42:45], v[54:55], off nt
	global_load_dwordx4 v[46:49], v[56:57], off nt
	s_nop 0
	global_load_dwordx4 v[50:53], v[58:59], off nt
	global_load_dwordx4 v[54:57], v[60:61], off nt
	s_nop 0
	global_load_dwordx4 v[58:61], v[62:63], off nt
	s_nop 0
	global_load_dwordx4 v[62:65], v[64:65], off nt
	s_mov_b32 s34, 0
	s_and_b64 vcc, exec, vcc
	v_readlane_b32 s37, v252, 17
	v_readlane_b32 s38, v252, 18
	v_readlane_b32 s39, v252, 19
	v_readlane_b32 s40, v252, 20
	v_readlane_b32 s41, v252, 21
	v_readlane_b32 s42, v252, 22
	v_readlane_b32 s43, v252, 23
	v_readlane_b32 s46, v252, 26
	v_readlane_b32 s47, v252, 27
	v_readlane_b32 s50, v252, 30
	v_readlane_b32 s51, v252, 31
	s_cbranch_vccnz .LBB0_540
	s_mov_b64 s[4:5], 0x80000
	v_lshl_add_u64 v[114:115], v[70:71], 0, s[4:5]
	s_mov_b64 s[4:5], 0x82000
	v_lshl_add_u64 v[112:113], v[70:71], 0, s[4:5]
	s_mov_b64 s[4:5], 0x84000
	v_lshl_add_u64 v[110:111], v[70:71], 0, s[4:5]
	s_mov_b64 s[4:5], 0x86000
	v_lshl_add_u64 v[108:109], v[70:71], 0, s[4:5]
	s_mov_b64 s[4:5], 0xa0000
	v_lshl_add_u64 v[106:107], v[70:71], 0, s[4:5]
	s_mov_b64 s[4:5], 0xa2000
	v_lshl_add_u64 v[104:105], v[70:71], 0, s[4:5]
	s_mov_b64 s[4:5], 0xa4000
	v_lshl_add_u64 v[102:103], v[70:71], 0, s[4:5]
	s_mov_b64 s[4:5], 0xa6000
	v_lshl_add_u64 v[98:99], v[70:71], 0, s[4:5]
	s_mov_b64 s[4:5], 0xc0000
	v_lshl_add_u64 v[94:95], v[70:71], 0, s[4:5]
	s_mov_b64 s[4:5], 0xc2000
	v_lshl_add_u64 v[90:91], v[70:71], 0, s[4:5]
	s_mov_b64 s[4:5], 0xc4000
	v_lshl_add_u64 v[86:87], v[70:71], 0, s[4:5]
	s_mov_b64 s[4:5], 0xc6000
	v_lshl_add_u64 v[82:83], v[70:71], 0, s[4:5]
	s_mov_b64 s[4:5], 0xe0000
	v_lshl_add_u64 v[78:79], v[70:71], 0, s[4:5]
	s_mov_b64 s[4:5], 0xe2000
	v_lshl_add_u64 v[74:75], v[70:71], 0, s[4:5]
	s_mov_b64 s[4:5], 0xe4000
	v_lshl_add_u64 v[72:73], v[70:71], 0, s[4:5]
	s_mov_b64 s[4:5], 0xe6000
	v_lshl_add_u64 v[70:71], v[70:71], 0, s[4:5]
	s_branch .LBB0_541

.LBB0_544:
	s_add_i32 s31, s34, 2
	s_min_i32 s6, s31, s13
	s_ashr_i32 s7, s6, 31
	s_lshr_b32 s7, s7, 30
	s_add_i32 s7, s6, s7
	s_lshr_b32 s8, s7, 2
	s_mul_i32 s8, s8, s99
	s_add_i32 s9, s8, s3
	s_mul_hi_i32 s8, s9, 0x2aaaaaab
	s_lshr_b32 s10, s8, 31
	s_ashr_i32 s8, s8, 7
	s_add_i32 s8, s8, s10
	s_mul_i32 s10, s8, 0x300
	s_and_b32 s7, s7, -4
	s_sub_i32 s36, s9, s10
	s_ashr_i32 s9, s8, 31
	s_sub_i32 s35, s6, s7
	s_cmpk_gt_i32 s36, 0x1ff
	s_mov_b64 s[6:7], -1
	s_cbranch_scc0 .LBB0_546
	v_readlane_b32 s40, v252, 16
	s_lshl_b64 s[6:7], s[8:9], 24
	v_readlane_b32 s52, v252, 28
	v_readlane_b32 s53, v252, 29
	s_add_u32 s6, s52, s6
	s_addc_u32 s7, s53, s7
	s_lshl_b32 s10, s36, 3
	s_and_b32 s10, s10, 0x700
	s_lshl_b32 s11, s35, 6
	s_add_i32 s37, s10, s11
	s_lshl_b32 s10, s36, 8
	s_and_b32 s10, s10, 0x1f00
	s_add_u32 s10, s6, s10
	v_readlane_b32 s41, v252, 17
	v_readlane_b32 s42, v252, 18
	v_readlane_b32 s43, v252, 19
	v_readlane_b32 s44, v252, 20
	v_readlane_b32 s45, v252, 21
	v_readlane_b32 s46, v252, 22
	v_readlane_b32 s47, v252, 23
	v_readlane_b32 s48, v252, 24
	v_readlane_b32 s49, v252, 25
	v_readlane_b32 s50, v252, 26
	v_readlane_b32 s51, v252, 27
	v_readlane_b32 s54, v252, 30
	v_readlane_b32 s55, v252, 31
	s_addc_u32 s11, s7, 0
	s_mov_b64 s[6:7], 0

; #define GAS __attribute__((address_space(1)))
; __device__ __forceinline__ void tr_load2(const float* W, int N, int fl, int hh, int lane, f32x4 (&v)[16]) {
;     const int nblk = N / 64, kb = fl / nblk, nb = fl % nblk, k0 = 64 * NHB * kb + 64 * hh, n0 = 64 * nb;
;     const int g = lane >> 4, c4 = (lane & 15) * 4;
; #pragma unroll
;     for (int i = 0; i < 16; ++i) v[i] = *(const GAS f32x4*)(W + (size_t)(k0 + 16 * (i >> 2) + 4 * g + (i & 3)) * N + n0 + c4);
; }
.LBB0_548:
	v_or_b32_e32 v130, s37, v1
	v_or_b32_e32 v154, 34, v130
	v_ashrrev_i32_e32 v155, 31, v154
	v_lshl_add_u64 v[132:133], s[10:11], 0, v[196:197]
	v_lshlrev_b64 v[154:155], s6, v[154:155]
	v_lshl_add_u64 v[210:211], v[132:133], 0, v[154:155]
	v_or_b32_e32 v154, 35, v130
	v_ashrrev_i32_e32 v155, 31, v154
	v_lshlrev_b64 v[154:155], s6, v[154:155]
	v_lshl_add_u64 v[216:217], v[132:133], 0, v[154:155]
	v_or_b32_e32 v154, 48, v130
	v_ashrrev_i32_e32 v155, 31, v154
	v_lshlrev_b64 v[154:155], s6, v[154:155]
	v_lshl_add_u64 v[218:219], v[132:133], 0, v[154:155]
	v_or_b32_e32 v154, 49, v130
	v_ashrrev_i32_e32 v155, 31, v154
	v_ashrrev_i32_e32 v131, 31, v130
	v_lshlrev_b64 v[154:155], s6, v[154:155]
	v_lshlrev_b64 v[134:135], s6, v[130:131]
	v_or_b32_e32 v136, 1, v130
	v_or_b32_e32 v138, 2, v130
	v_or_b32_e32 v140, 3, v130
	v_or_b32_e32 v142, 16, v130
	v_or_b32_e32 v144, 17, v130
	v_or_b32_e32 v146, 18, v130
	v_or_b32_e32 v148, 19, v130
	v_or_b32_e32 v150, 32, v130
	v_or_b32_e32 v152, 33, v130
	v_lshl_add_u64 v[220:221], v[132:133], 0, v[154:155]
	v_or_b32_e32 v154, 50, v130
	v_or_b32_e32 v130, 51, v130
	v_ashrrev_i32_e32 v137, 31, v136
	v_ashrrev_i32_e32 v139, 31, v138
	v_ashrrev_i32_e32 v141, 31, v140
	v_ashrrev_i32_e32 v143, 31, v142
	v_ashrrev_i32_e32 v145, 31, v144
	v_ashrrev_i32_e32 v147, 31, v146
	v_ashrrev_i32_e32 v149, 31, v148
	v_ashrrev_i32_e32 v151, 31, v150
	v_ashrrev_i32_e32 v153, 31, v152
	v_ashrrev_i32_e32 v131, 31, v130
	v_lshlrev_b64 v[136:137], s6, v[136:137]
	v_lshlrev_b64 v[138:139], s6, v[138:139]
	v_lshlrev_b64 v[140:141], s6, v[140:141]
	v_lshlrev_b64 v[142:143], s6, v[142:143]
	v_lshlrev_b64 v[144:145], s6, v[144:145]
	v_lshlrev_b64 v[146:147], s6, v[146:147]
	v_lshlrev_b64 v[148:149], s6, v[148:149]
	v_lshlrev_b64 v[150:151], s6, v[150:151]
	v_lshlrev_b64 v[152:153], s6, v[152:153]
	v_ashrrev_i32_e32 v155, 31, v154
	v_lshlrev_b64 v[130:131], s6, v[130:131]
	v_lshl_add_u64 v[134:135], v[132:133], 0, v[134:135]
	v_lshl_add_u64 v[136:137], v[132:133], 0, v[136:137]
	v_lshl_add_u64 v[138:139], v[132:133], 0, v[138:139]
	v_lshl_add_u64 v[140:141], v[132:133], 0, v[140:141]
	v_lshl_add_u64 v[142:143], v[132:133], 0, v[142:143]
	v_lshl_add_u64 v[144:145], v[132:133], 0, v[144:145]
	v_lshl_add_u64 v[146:147], v[132:133], 0, v[146:147]
	v_lshl_add_u64 v[148:149], v[132:133], 0, v[148:149]
	v_lshl_add_u64 v[150:151], v[132:133], 0, v[150:151]
	v_lshl_add_u64 v[152:153], v[132:133], 0, v[152:153]
	v_lshlrev_b64 v[154:155], s6, v[154:155]
	v_lshl_add_u64 v[130:131], v[132:133], 0, v[130:131]
	v_lshl_add_u64 v[222:223], v[132:133], 0, v[154:155]
	global_load_dwordx4 v[190:193], v[134:135], off nt
	global_load_dwordx4 v[186:189], v[136:137], off nt
	global_load_dwordx4 v[182:185], v[138:139], off nt
	global_load_dwordx4 v[178:181], v[140:141], off nt
	global_load_dwordx4 v[174:177], v[142:143], off nt
	global_load_dwordx4 v[170:173], v[144:145], off nt
	global_load_dwordx4 v[166:169], v[146:147], off nt
	global_load_dwordx4 v[162:165], v[148:149], off nt
	global_load_dwordx4 v[158:161], v[150:151], off nt
	global_load_dwordx4 v[154:157], v[152:153], off nt
	s_nop 0
	global_load_dwordx4 v[150:153], v[210:211], off nt
	global_load_dwordx4 v[146:149], v[216:217], off nt
	global_load_dwordx4 v[142:145], v[218:219], off nt
	global_load_dwordx4 v[138:141], v[220:221], off nt
	global_load_dwordx4 v[134:137], v[222:223], off nt
	s_nop 0
	global_load_dwordx4 v[130:133], v[130:131], off nt
	s_waitcnt vmcnt(0)
; #define LAS __attribute__((address_space(3)))
; __device__ __forceinline__ unsigned pk4_fp8_nc(float a, float b, float c, float d) { int w = 0; w = __builtin_amdgcn_cvt_pk_fp8_f32(a, b, w, false); w = __builtin_amdgcn_cvt_pk_fp8_f32(c, d, w, true); return (unsigned)w; }
; __device__ __forceinline__ void tr_half(const f32x4 (&v)[16], int hh, LAS unsigned* img, int lane, float scale) {
;     const int g = lane >> 4, m = lane & 15;
; #pragma unroll
;     for (int j = 0; j < 4; ++j) { const f32x4 a = v[4 * j] * scale, b = v[4 * j + 1] * scale, c = v[4 * j + 2] * scale, d = v[4 * j + 3] * scale;
;         const int dwi = (16 * hh + 4 * j + g) ^ ((m & 7) << 2);
;         img[(4 * m + 0) * (16 * NHB) + dwi] = pk4_fp8_nc(a.x, b.x, c.x, d.x); img[(4 * m + 1) * (16 * NHB) + dwi] = pk4_fp8_nc(a.y, b.y, c.y, d.y);
;         img[(4 * m + 2) * (16 * NHB) + dwi] = pk4_fp8_nc(a.z, b.z, c.z, d.z); img[(4 * m + 3) * (16 * NHB) + dwi] = pk4_fp8_nc(a.w, b.w, c.w, d.w); }
; }
	v_pk_mul_f32 v[62:63], v[62:63], s[2:3] op_sel_hi:[1,0]
	v_pk_mul_f32 v[58:59], v[58:59], s[2:3] op_sel_hi:[1,0]
	v_mov_b32_e32 v211, v197
	v_cvt_pk_fp8_f32 v211, v62, v58
	v_mov_b32_e32 v58, v197
	v_pk_mul_f32 v[64:65], v[64:65], s[2:3] op_sel_hi:[1,0]
	v_pk_mul_f32 v[60:61], v[60:61], s[2:3] op_sel_hi:[1,0]
	v_cvt_pk_fp8_f32 v58, v63, v59
	v_mov_b32_e32 v59, v197
	v_cvt_pk_fp8_f32 v59, v64, v60
	v_mov_b32_e32 v60, v197
	v_cvt_pk_fp8_f32 v60, v65, v61
	v_pk_mul_f32 v[54:55], v[54:55], s[2:3] op_sel_hi:[1,0]
	v_pk_mul_f32 v[50:51], v[50:51], s[2:3] op_sel_hi:[1,0]
	s_and_b32 s6, s34, 3
	v_pk_mul_f32 v[56:57], v[56:57], s[2:3] op_sel_hi:[1,0]
	v_pk_mul_f32 v[52:53], v[52:53], s[2:3] op_sel_hi:[1,0]
	v_cvt_pk_fp8_f32 v211, v54, v50 op_sel:[0,0,1]
	v_cvt_pk_fp8_f32 v58, v55, v51 op_sel:[0,0,1]
	s_lshl_b32 s7, s6, 4
	v_cvt_pk_fp8_f32 v59, v56, v52 op_sel:[0,0,1]
	v_cvt_pk_fp8_f32 v60, v57, v53 op_sel:[0,0,1]
	v_bitop3_b32 v50, s7, v203, v201 bitop3:0x36
	v_lshl_add_u32 v50, v50, 2, v212
	ds_write2st64_b32 v50, v211, v58 offset1:1
	ds_write2st64_b32 v50, v59, v60 offset0:2 offset1:3
	v_pk_mul_f32 v[46:47], v[46:47], s[2:3] op_sel_hi:[1,0]
	v_pk_mul_f32 v[42:43], v[42:43], s[2:3] op_sel_hi:[1,0]
	v_mov_b32_e32 v50, v197
	v_cvt_pk_fp8_f32 v50, v46, v42
	v_mov_b32_e32 v42, v197
	v_pk_mul_f32 v[48:49], v[48:49], s[2:3] op_sel_hi:[1,0]
	v_pk_mul_f32 v[44:45], v[44:45], s[2:3] op_sel_hi:[1,0]
	v_cvt_pk_fp8_f32 v42, v47, v43
	v_mov_b32_e32 v43, v197
	v_cvt_pk_fp8_f32 v43, v48, v44
	v_mov_b32_e32 v44, v197
	v_cvt_pk_fp8_f32 v44, v49, v45
	v_pk_mul_f32 v[38:39], v[38:39], s[2:3] op_sel_hi:[1,0]
	v_pk_mul_f32 v[34:35], v[34:35], s[2:3] op_sel_hi:[1,0]
	v_pk_mul_f32 v[40:41], v[40:41], s[2:3] op_sel_hi:[1,0]
	v_pk_mul_f32 v[36:37], v[36:37], s[2:3] op_sel_hi:[1,0]
	v_cvt_pk_fp8_f32 v50, v38, v34 op_sel:[0,0,1]
	v_cvt_pk_fp8_f32 v42, v39, v35 op_sel:[0,0,1]
	v_or_b32_e32 v210, s7, v201
	v_cvt_pk_fp8_f32 v43, v40, v36 op_sel:[0,0,1]
	v_cvt_pk_fp8_f32 v44, v41, v37 op_sel:[0,0,1]
	v_bitop3_b32 v34, v210, v203, 4 bitop3:0x36
	v_lshl_add_u32 v34, v34, 2, v212
	ds_write2st64_b32 v34, v50, v42 offset1:1
	ds_write2st64_b32 v34, v43, v44 offset0:2 offset1:3
	v_pk_mul_f32 v[30:31], v[30:31], s[2:3] op_sel_hi:[1,0]
	v_pk_mul_f32 v[26:27], v[26:27], s[2:3] op_sel_hi:[1,0]
	v_mov_b32_e32 v34, v197
	v_cvt_pk_fp8_f32 v34, v30, v26
	v_mov_b32_e32 v26, v197
	v_cvt_pk_fp8_f32 v26, v31, v27
	v_pk_mul_f32 v[22:23], v[22:23], s[2:3] op_sel_hi:[1,0]
	v_pk_mul_f32 v[18:19], v[18:19], s[2:3] op_sel_hi:[1,0]
	v_pk_mul_f32 v[14:15], v[14:15], s[2:3] op_sel_hi:[1,0]
	v_cvt_pk_fp8_f32 v26, v23, v19 op_sel:[0,0,1]
	v_pk_mul_f32 v[10:11], v[10:11], s[2:3] op_sel_hi:[1,0]
	v_mov_b32_e32 v19, v197
	v_pk_mul_f32 v[32:33], v[32:33], s[2:3] op_sel_hi:[1,0]
	v_pk_mul_f32 v[28:29], v[28:29], s[2:3] op_sel_hi:[1,0]
	v_mov_b32_e32 v27, v197
	v_cvt_pk_fp8_f32 v19, v14, v10
	v_mov_b32_e32 v10, v197
	v_cvt_pk_fp8_f32 v27, v32, v28
	v_mov_b32_e32 v28, v197
	v_pk_mul_f32 v[16:17], v[16:17], s[2:3] op_sel_hi:[1,0]
	v_pk_mul_f32 v[12:13], v[12:13], s[2:3] op_sel_hi:[1,0]
	v_cvt_pk_fp8_f32 v10, v15, v11
	v_mov_b32_e32 v11, v197
	v_cvt_pk_fp8_f32 v28, v33, v29
	v_cvt_pk_fp8_f32 v11, v16, v12
	v_mov_b32_e32 v12, v197
	v_cvt_pk_fp8_f32 v12, v17, v13
	v_pk_mul_f32 v[24:25], v[24:25], s[2:3] op_sel_hi:[1,0]
	v_pk_mul_f32 v[20:21], v[20:21], s[2:3] op_sel_hi:[1,0]
	v_cvt_pk_fp8_f32 v34, v22, v18 op_sel:[0,0,1]
	v_cvt_pk_fp8_f32 v27, v24, v20 op_sel:[0,0,1]
	v_cvt_pk_fp8_f32 v28, v25, v21 op_sel:[0,0,1]
	v_pk_mul_f32 v[8:9], v[8:9], s[2:3] op_sel_hi:[1,0]
	v_pk_mul_f32 v[6:7], v[6:7], s[2:3] op_sel_hi:[1,0]
	v_pk_mul_f32 v[4:5], v[4:5], s[2:3] op_sel_hi:[1,0]
	v_pk_mul_f32 v[2:3], v[2:3], s[2:3] op_sel_hi:[1,0]
	v_bitop3_b32 v18, v210, v203, 8 bitop3:0x36
	v_cvt_pk_fp8_f32 v19, v6, v2 op_sel:[0,0,1]
	v_cvt_pk_fp8_f32 v10, v7, v3 op_sel:[0,0,1]
	v_cvt_pk_fp8_f32 v11, v8, v4 op_sel:[0,0,1]
	v_cvt_pk_fp8_f32 v12, v9, v5 op_sel:[0,0,1]
	v_lshl_add_u32 v18, v18, 2, v212
	ds_write2st64_b32 v18, v34, v26 offset1:1
	ds_write2st64_b32 v18, v27, v28 offset0:2 offset1:3
	v_bitop3_b32 v18, v210, v203, 12 bitop3:0x36
	v_lshl_add_u32 v2, v18, 2, v212
	s_cmp_lg_u32 s6, 3
	ds_write2st64_b32 v2, v19, v10 offset1:1
	ds_write2st64_b32 v2, v11, v12 offset0:2 offset1:3
	s_cbranch_scc1 .LBB0_557
	s_lshr_b32 s6, s34, 2
	s_mul_i32 s6, s6, s99
	s_add_i32 s7, s6, s3
	s_mul_hi_i32 s6, s7, 0x2aaaaaab
	s_lshr_b32 s8, s6, 31
	s_ashr_i32 s6, s6, 7
	s_add_i32 s6, s6, s8
	s_mul_i32 s8, s6, 0x300
	s_sub_i32 s10, s7, s8
	s_ashr_i32 s7, s6, 31
	s_cmpk_gt_i32 s10, 0x1ff
	s_mov_b64 s[8:9], -1
	s_cbranch_scc0 .LBB0_553
	s_and_b32 s35, s10, 31
	s_lshl_b32 s9, s10, 3
	s_lshl_b64 s[38:39], s[6:7], 22
	s_lshl_b32 s35, s35, 17
	s_lshl_b64 s[36:37], s[6:7], 11
	s_and_b32 s9, s9, 0x700
	s_lshl_b32 s11, s10, 6
	s_or_b32 s35, s38, s35
	s_and_b32 s11, s11, 0x7c0
	s_waitcnt lgkmcnt(0)
	s_or_b32 s38, s35, s9
	v_or_b32_e32 v4, s36, v202
	v_mov_b32_e32 v5, s37
	v_or_b32_e32 v4, s11, v4
	s_add_u32 s36, s29, s9
	v_lshlrev_b64 v[4:5], 11, v[4:5]
	s_addc_u32 s37, s72, 0
	s_mov_b32 s8, 3
	v_lshl_add_u64 v[2:3], v[204:205], 0, s[38:39]
	v_lshl_add_u64 v[4:5], s[36:37], 0, v[4:5]
	v_mov_b32_e32 v6, v214

; #define CONV_LD(ss_, buf_) { const int sc_ = (ss_) < nhalf ? (ss_) : nhalf - 1; const int fi_ = cw + (sc_ / NHB) * STRIDE, e_ = fi_ / FPE, r_ = fi_ % FPE; \
;                 if (r_ < F1) tr_load2(w1 + (size_t)e_ * D * 4096, 4096, r_, sc_ % NHB, lane, buf_); else tr_load2(w2 + (size_t)e_ * DFF * D, D, r_ - F1, sc_ % NHB, lane, buf_); }
; __global__ void __launch_bounds__(NTHR, 2) mk_fwd(Args args) {
;     ...
;             if (nhalf > 0) { CONV_LD(0, va); CONV_LD(1, vb2);
;                 for (;;) { CONV_STEP(va, vc); if (s >= nhalf) break; CONV_STEP(vb2, va); if (s >= nhalf) break; CONV_STEP(vc, vb2); if (s >= nhalf) break; } }
.LBB0_557:
	s_add_i32 s36, s34, 1
	s_cmp_ge_u32 s36, s12
	s_mov_b64 s[6:7], -1
	s_cbranch_scc1 .LBB0_543
	s_add_i32 s35, s34, 3
	s_min_i32 s6, s35, s13
	s_ashr_i32 s7, s6, 31
	s_lshr_b32 s7, s7, 30
	s_add_i32 s7, s6, s7
	s_lshr_b32 s8, s7, 2
	s_mul_i32 s8, s8, s99
	s_add_i32 s9, s8, s3
	s_mul_hi_i32 s8, s9, 0x2aaaaaab
	s_lshr_b32 s10, s8, 31
	s_ashr_i32 s8, s8, 7
	s_add_i32 s8, s8, s10
	s_mul_i32 s10, s8, 0x300
	s_and_b32 s7, s7, -4
	s_sub_i32 s38, s9, s10
	s_ashr_i32 s9, s8, 31
	s_sub_i32 s37, s6, s7
	s_cmpk_gt_i32 s38, 0x1ff
	s_mov_b64 s[6:7], -1
	s_cbranch_scc0 .LBB0_560
	v_readlane_b32 s40, v252, 16
	s_lshl_b64 s[6:7], s[8:9], 24
	v_readlane_b32 s52, v252, 28
	v_readlane_b32 s53, v252, 29
	s_add_u32 s6, s52, s6
	s_addc_u32 s7, s53, s7
	s_lshl_b32 s10, s38, 3
	s_and_b32 s10, s10, 0x700
	s_lshl_b32 s11, s37, 6
	s_add_i32 s39, s10, s11
	s_lshl_b32 s10, s38, 8
	s_and_b32 s10, s10, 0x1f00
	s_add_u32 s10, s6, s10
	v_readlane_b32 s41, v252, 17
	v_readlane_b32 s42, v252, 18
	v_readlane_b32 s43, v252, 19
	v_readlane_b32 s44, v252, 20
	v_readlane_b32 s45, v252, 21
	v_readlane_b32 s46, v252, 22
	v_readlane_b32 s47, v252, 23
	v_readlane_b32 s48, v252, 24
	v_readlane_b32 s49, v252, 25
	v_readlane_b32 s50, v252, 26
	v_readlane_b32 s51, v252, 27
	v_readlane_b32 s54, v252, 30
	v_readlane_b32 s55, v252, 31
	s_addc_u32 s11, s7, 0
	s_mov_b64 s[6:7], 0

; #define GAS __attribute__((address_space(1)))
; #define LAS __attribute__((address_space(3)))
; __device__ __forceinline__ unsigned pk4_fp8_nc(float a, float b, float c, float d) { int w = 0; w = __builtin_amdgcn_cvt_pk_fp8_f32(a, b, w, false); w = __builtin_amdgcn_cvt_pk_fp8_f32(c, d, w, true); return (unsigned)w; }
; __device__ __forceinline__ void tr_load2(const float* W, int N, int fl, int hh, int lane, f32x4 (&v)[16]) {
;     const int nblk = N / 64, kb = fl / nblk, nb = fl % nblk, k0 = 64 * NHB * kb + 64 * hh, n0 = 64 * nb;
;     const int g = lane >> 4, c4 = (lane & 15) * 4;
; #pragma unroll
;     for (int i = 0; i < 16; ++i) v[i] = *(const GAS f32x4*)(W + (size_t)(k0 + 16 * (i >> 2) + 4 * g + (i & 3)) * N + n0 + c4);
; }
; __device__ __forceinline__ void tr_half(const f32x4 (&v)[16], int hh, LAS unsigned* img, int lane, float scale) {
;     const int g = lane >> 4, m = lane & 15;
; #pragma unroll
;     for (int j = 0; j < 4; ++j) { const f32x4 a = v[4 * j] * scale, b = v[4 * j + 1] * scale, c = v[4 * j + 2] * scale, d = v[4 * j + 3] * scale;
;         const int dwi = (16 * hh + 4 * j + g) ^ ((m & 7) << 2);
;         img[(4 * m + 0) * (16 * NHB) + dwi] = pk4_fp8_nc(a.x, b.x, c.x, d.x); img[(4 * m + 1) * (16 * NHB) + dwi] = pk4_fp8_nc(a.y, b.y, c.y, d.y);
;         img[(4 * m + 2) * (16 * NHB) + dwi] = pk4_fp8_nc(a.z, b.z, c.z, d.z); img[(4 * m + 3) * (16 * NHB) + dwi] = pk4_fp8_nc(a.w, b.w, c.w, d.w); }
; }
.LBB0_562:
	v_or_b32_e32 v2, s39, v1
	v_lshlrev_b32_e32 v210, 2, v200
	v_mov_b32_e32 v211, v197
	v_ashrrev_i32_e32 v3, 31, v2
	v_lshl_add_u64 v[4:5], s[10:11], 0, v[210:211]
	v_lshlrev_b64 v[6:7], s6, v[2:3]
	v_lshl_add_u64 v[62:63], v[4:5], 0, v[6:7]
	v_or_b32_e32 v6, 1, v2
	v_ashrrev_i32_e32 v7, 31, v6
	v_lshlrev_b64 v[6:7], s6, v[6:7]
	v_lshl_add_u64 v[58:59], v[4:5], 0, v[6:7]
	v_or_b32_e32 v6, 2, v2
	v_ashrrev_i32_e32 v7, 31, v6
	v_lshlrev_b64 v[6:7], s6, v[6:7]
	v_lshl_add_u64 v[54:55], v[4:5], 0, v[6:7]
	v_or_b32_e32 v6, 3, v2
	v_ashrrev_i32_e32 v7, 31, v6
	v_lshlrev_b64 v[6:7], s6, v[6:7]
	v_lshl_add_u64 v[50:51], v[4:5], 0, v[6:7]
	v_or_b32_e32 v6, 16, v2
	v_ashrrev_i32_e32 v7, 31, v6
	v_lshlrev_b64 v[6:7], s6, v[6:7]
	v_lshl_add_u64 v[46:47], v[4:5], 0, v[6:7]
	v_or_b32_e32 v6, 17, v2
	v_ashrrev_i32_e32 v7, 31, v6
	v_lshlrev_b64 v[6:7], s6, v[6:7]
	v_lshl_add_u64 v[42:43], v[4:5], 0, v[6:7]
	v_or_b32_e32 v6, 18, v2
	v_ashrrev_i32_e32 v7, 31, v6
	v_lshlrev_b64 v[6:7], s6, v[6:7]
	v_lshl_add_u64 v[38:39], v[4:5], 0, v[6:7]
	v_or_b32_e32 v6, 19, v2
	v_ashrrev_i32_e32 v7, 31, v6
	v_lshlrev_b64 v[6:7], s6, v[6:7]
	v_lshl_add_u64 v[34:35], v[4:5], 0, v[6:7]
	v_or_b32_e32 v6, 32, v2
	v_ashrrev_i32_e32 v7, 31, v6
	v_lshlrev_b64 v[6:7], s6, v[6:7]
	v_lshl_add_u64 v[30:31], v[4:5], 0, v[6:7]
	v_or_b32_e32 v6, 33, v2
	v_ashrrev_i32_e32 v7, 31, v6
	v_lshlrev_b64 v[6:7], s6, v[6:7]
	v_lshl_add_u64 v[26:27], v[4:5], 0, v[6:7]
	v_or_b32_e32 v6, 34, v2
	v_ashrrev_i32_e32 v7, 31, v6
	v_lshlrev_b64 v[6:7], s6, v[6:7]
	v_lshl_add_u64 v[22:23], v[4:5], 0, v[6:7]
	v_or_b32_e32 v6, 35, v2
	v_ashrrev_i32_e32 v7, 31, v6
	v_lshlrev_b64 v[6:7], s6, v[6:7]
	v_lshl_add_u64 v[18:19], v[4:5], 0, v[6:7]
	v_or_b32_e32 v6, 48, v2
	v_ashrrev_i32_e32 v7, 31, v6
	v_lshlrev_b64 v[6:7], s6, v[6:7]
	v_lshl_add_u64 v[14:15], v[4:5], 0, v[6:7]
	v_or_b32_e32 v6, 49, v2
	v_ashrrev_i32_e32 v7, 31, v6
	v_lshlrev_b64 v[6:7], s6, v[6:7]
	v_lshl_add_u64 v[10:11], v[4:5], 0, v[6:7]
	v_or_b32_e32 v6, 50, v2
	v_or_b32_e32 v2, 51, v2
	v_ashrrev_i32_e32 v7, 31, v6
	v_ashrrev_i32_e32 v3, 31, v2
	v_lshlrev_b64 v[6:7], s6, v[6:7]
	v_lshlrev_b64 v[2:3], s6, v[2:3]
	v_lshl_add_u64 v[6:7], v[4:5], 0, v[6:7]
	v_lshl_add_u64 v[2:3], v[4:5], 0, v[2:3]
	global_load_dwordx4 v[2:5], v[2:3], off nt
	s_nop 0
	global_load_dwordx4 v[6:9], v[6:7], off nt
	s_nop 0
	global_load_dwordx4 v[10:13], v[10:11], off nt
	s_nop 0
	global_load_dwordx4 v[14:17], v[14:15], off nt
	s_nop 0
	global_load_dwordx4 v[18:21], v[18:19], off nt
	s_nop 0
	global_load_dwordx4 v[22:25], v[22:23], off nt
	s_nop 0
	global_load_dwordx4 v[26:29], v[26:27], off nt
	s_nop 0
	global_load_dwordx4 v[30:33], v[30:31], off nt
	s_nop 0
	global_load_dwordx4 v[34:37], v[34:35], off nt
	s_nop 0
	global_load_dwordx4 v[38:41], v[38:39], off nt
	s_nop 0
	global_load_dwordx4 v[42:45], v[42:43], off nt
	s_nop 0
	global_load_dwordx4 v[46:49], v[46:47], off nt
	s_nop 0
	global_load_dwordx4 v[50:53], v[50:51], off nt
	s_nop 0
	global_load_dwordx4 v[54:57], v[54:55], off nt
	s_nop 0
	global_load_dwordx4 v[58:61], v[58:59], off nt
	s_nop 0
	global_load_dwordx4 v[62:65], v[62:63], off nt
	v_pk_mul_f32 v[126:127], v[126:127], s[2:3] op_sel_hi:[1,0]
	v_pk_mul_f32 v[122:123], v[122:123], s[2:3] op_sel_hi:[1,0]
	v_mov_b32_e32 v215, v197
	v_cvt_pk_fp8_f32 v215, v126, v122
	v_mov_b32_e32 v122, v197
	v_pk_mul_f32 v[128:129], v[128:129], s[2:3] op_sel_hi:[1,0]
	v_pk_mul_f32 v[124:125], v[124:125], s[2:3] op_sel_hi:[1,0]
	v_cvt_pk_fp8_f32 v122, v127, v123
	v_mov_b32_e32 v123, v197
	v_cvt_pk_fp8_f32 v123, v128, v124
	v_mov_b32_e32 v124, v197
	v_cvt_pk_fp8_f32 v124, v129, v125
	v_pk_mul_f32 v[118:119], v[118:119], s[2:3] op_sel_hi:[1,0]
	v_pk_mul_f32 v[114:115], v[114:115], s[2:3] op_sel_hi:[1,0]
	s_and_b32 s6, s36, 3
	v_pk_mul_f32 v[120:121], v[120:121], s[2:3] op_sel_hi:[1,0]
	v_pk_mul_f32 v[116:117], v[116:117], s[2:3] op_sel_hi:[1,0]
	v_cvt_pk_fp8_f32 v215, v118, v114 op_sel:[0,0,1]
	v_cvt_pk_fp8_f32 v122, v119, v115 op_sel:[0,0,1]
	s_lshl_b32 s7, s6, 4
	v_cvt_pk_fp8_f32 v123, v120, v116 op_sel:[0,0,1]
	v_cvt_pk_fp8_f32 v124, v121, v117 op_sel:[0,0,1]
	v_bitop3_b32 v114, s7, v203, v201 bitop3:0x36
	v_lshl_add_u32 v114, v114, 2, v212
	ds_write2st64_b32 v114, v215, v122 offset1:1
; #define LAS __attribute__((address_space(3)))
; __device__ __forceinline__ unsigned pk4_fp8_nc(float a, float b, float c, float d) { int w = 0; w = __builtin_amdgcn_cvt_pk_fp8_f32(a, b, w, false); w = __builtin_amdgcn_cvt_pk_fp8_f32(c, d, w, true); return (unsigned)w; }
; __device__ __forceinline__ void tr_half(const f32x4 (&v)[16], int hh, LAS unsigned* img, int lane, float scale) {
;     const int g = lane >> 4, m = lane & 15;
; #pragma unroll
;     for (int j = 0; j < 4; ++j) { const f32x4 a = v[4 * j] * scale, b = v[4 * j + 1] * scale, c = v[4 * j + 2] * scale, d = v[4 * j + 3] * scale;
;         const int dwi = (16 * hh + 4 * j + g) ^ ((m & 7) << 2);
;         img[(4 * m + 0) * (16 * NHB) + dwi] = pk4_fp8_nc(a.x, b.x, c.x, d.x); img[(4 * m + 1) * (16 * NHB) + dwi] = pk4_fp8_nc(a.y, b.y, c.y, d.y);
;         img[(4 * m + 2) * (16 * NHB) + dwi] = pk4_fp8_nc(a.z, b.z, c.z, d.z); img[(4 * m + 3) * (16 * NHB) + dwi] = pk4_fp8_nc(a.w, b.w, c.w, d.w); }
; }
	ds_write2st64_b32 v114, v123, v124 offset0:2 offset1:3
	v_pk_mul_f32 v[110:111], v[110:111], s[2:3] op_sel_hi:[1,0]
	v_pk_mul_f32 v[106:107], v[106:107], s[2:3] op_sel_hi:[1,0]
	v_mov_b32_e32 v114, v197
	v_cvt_pk_fp8_f32 v114, v110, v106
	v_mov_b32_e32 v106, v197
	v_pk_mul_f32 v[112:113], v[112:113], s[2:3] op_sel_hi:[1,0]
	v_pk_mul_f32 v[108:109], v[108:109], s[2:3] op_sel_hi:[1,0]
	v_cvt_pk_fp8_f32 v106, v111, v107
	v_mov_b32_e32 v107, v197
	v_cvt_pk_fp8_f32 v107, v112, v108
	v_mov_b32_e32 v108, v197
	v_cvt_pk_fp8_f32 v108, v113, v109
	v_pk_mul_f32 v[102:103], v[102:103], s[2:3] op_sel_hi:[1,0]
	v_pk_mul_f32 v[98:99], v[98:99], s[2:3] op_sel_hi:[1,0]
	v_pk_mul_f32 v[104:105], v[104:105], s[2:3] op_sel_hi:[1,0]
	v_pk_mul_f32 v[100:101], v[100:101], s[2:3] op_sel_hi:[1,0]
	v_cvt_pk_fp8_f32 v114, v102, v98 op_sel:[0,0,1]
	v_cvt_pk_fp8_f32 v106, v103, v99 op_sel:[0,0,1]
	v_or_b32_e32 v211, s7, v201
	v_cvt_pk_fp8_f32 v107, v104, v100 op_sel:[0,0,1]
	v_cvt_pk_fp8_f32 v108, v105, v101 op_sel:[0,0,1]
	v_bitop3_b32 v98, v211, v203, 4 bitop3:0x36
	v_lshl_add_u32 v98, v98, 2, v212
	ds_write2st64_b32 v98, v114, v106 offset1:1
	ds_write2st64_b32 v98, v107, v108 offset0:2 offset1:3
	v_pk_mul_f32 v[94:95], v[94:95], s[2:3] op_sel_hi:[1,0]
	v_pk_mul_f32 v[90:91], v[90:91], s[2:3] op_sel_hi:[1,0]
	v_mov_b32_e32 v98, v197
	v_cvt_pk_fp8_f32 v98, v94, v90
	v_mov_b32_e32 v90, v197
	v_cvt_pk_fp8_f32 v90, v95, v91
	v_pk_mul_f32 v[86:87], v[86:87], s[2:3] op_sel_hi:[1,0]
	v_pk_mul_f32 v[82:83], v[82:83], s[2:3] op_sel_hi:[1,0]
	v_pk_mul_f32 v[78:79], v[78:79], s[2:3] op_sel_hi:[1,0]
	v_cvt_pk_fp8_f32 v90, v87, v83 op_sel:[0,0,1]
	v_pk_mul_f32 v[74:75], v[74:75], s[2:3] op_sel_hi:[1,0]
	v_mov_b32_e32 v83, v197
	v_pk_mul_f32 v[96:97], v[96:97], s[2:3] op_sel_hi:[1,0]
	v_pk_mul_f32 v[92:93], v[92:93], s[2:3] op_sel_hi:[1,0]
	v_mov_b32_e32 v91, v197
	v_cvt_pk_fp8_f32 v83, v78, v74
	v_mov_b32_e32 v74, v197
	v_cvt_pk_fp8_f32 v91, v96, v92
	v_mov_b32_e32 v92, v197
	v_pk_mul_f32 v[80:81], v[80:81], s[2:3] op_sel_hi:[1,0]
	v_pk_mul_f32 v[76:77], v[76:77], s[2:3] op_sel_hi:[1,0]
	v_cvt_pk_fp8_f32 v74, v79, v75
	v_mov_b32_e32 v75, v197
	v_cvt_pk_fp8_f32 v92, v97, v93
	v_cvt_pk_fp8_f32 v75, v80, v76
	v_mov_b32_e32 v76, v197
	v_cvt_pk_fp8_f32 v76, v81, v77
	v_pk_mul_f32 v[88:89], v[88:89], s[2:3] op_sel_hi:[1,0]
	v_pk_mul_f32 v[84:85], v[84:85], s[2:3] op_sel_hi:[1,0]
	v_cvt_pk_fp8_f32 v98, v86, v82 op_sel:[0,0,1]
	v_cvt_pk_fp8_f32 v91, v88, v84 op_sel:[0,0,1]
	v_cvt_pk_fp8_f32 v92, v89, v85 op_sel:[0,0,1]
	v_pk_mul_f32 v[72:73], v[72:73], s[2:3] op_sel_hi:[1,0]
	v_pk_mul_f32 v[70:71], v[70:71], s[2:3] op_sel_hi:[1,0]
	v_pk_mul_f32 v[68:69], v[68:69], s[2:3] op_sel_hi:[1,0]
	v_pk_mul_f32 v[66:67], v[66:67], s[2:3] op_sel_hi:[1,0]
	v_bitop3_b32 v82, v211, v203, 8 bitop3:0x36
	v_cvt_pk_fp8_f32 v83, v70, v66 op_sel:[0,0,1]
	v_cvt_pk_fp8_f32 v74, v71, v67 op_sel:[0,0,1]
	v_cvt_pk_fp8_f32 v75, v72, v68 op_sel:[0,0,1]
	v_cvt_pk_fp8_f32 v76, v73, v69 op_sel:[0,0,1]
	v_lshl_add_u32 v82, v82, 2, v212
	ds_write2st64_b32 v82, v98, v90 offset1:1
	ds_write2st64_b32 v82, v91, v92 offset0:2 offset1:3
	v_bitop3_b32 v82, v211, v203, 12 bitop3:0x36
	v_lshl_add_u32 v66, v82, 2, v212
	s_cmp_lg_u32 s6, 3
	ds_write2st64_b32 v66, v83, v74 offset1:1
	ds_write2st64_b32 v66, v75, v76 offset0:2 offset1:3
	s_cbranch_scc1 .LBB0_571
	s_lshr_b32 s6, s36, 2
	s_mul_i32 s6, s6, s99
	s_add_i32 s7, s6, s3
	s_mul_hi_i32 s6, s7, 0x2aaaaaab
	s_lshr_b32 s8, s6, 31
	s_ashr_i32 s6, s6, 7
	s_add_i32 s6, s6, s8
	s_mul_i32 s8, s6, 0x300
	s_sub_i32 s10, s7, s8
	s_ashr_i32 s7, s6, 31
	s_cmpk_gt_i32 s10, 0x1ff
	s_mov_b64 s[8:9], -1
	s_cbranch_scc0 .LBB0_567
	s_and_b32 s40, s10, 31
	s_lshl_b32 s9, s10, 3
	s_lshl_b64 s[38:39], s[6:7], 22
	s_lshl_b32 s40, s40, 17
	s_lshl_b64 s[36:37], s[6:7], 11
	s_and_b32 s9, s9, 0x700
	s_lshl_b32 s11, s10, 6
	s_or_b32 s38, s38, s40
	s_and_b32 s11, s11, 0x7c0
	s_waitcnt lgkmcnt(0)
	s_or_b32 s38, s38, s9
	v_or_b32_e32 v68, s36, v202
	v_mov_b32_e32 v69, s37
	v_or_b32_e32 v68, s11, v68
	s_add_u32 s36, s29, s9
	v_lshlrev_b64 v[68:69], 11, v[68:69]
	s_addc_u32 s37, s72, 0
	s_mov_b32 s8, 3
	v_lshl_add_u64 v[66:67], v[204:205], 0, s[38:39]
	v_lshl_add_u64 v[68:69], s[36:37], 0, v[68:69]
	v_mov_b32_e32 v70, v214

; #define CONV_LD(ss_, buf_) { const int sc_ = (ss_) < nhalf ? (ss_) : nhalf - 1; const int fi_ = cw + (sc_ / NHB) * STRIDE, e_ = fi_ / FPE, r_ = fi_ % FPE; \
;                 if (r_ < F1) tr_load2(w1 + (size_t)e_ * D * 4096, 4096, r_, sc_ % NHB, lane, buf_); else tr_load2(w2 + (size_t)e_ * DFF * D, D, r_ - F1, sc_ % NHB, lane, buf_); }
; __global__ void __launch_bounds__(NTHR, 2) mk_fwd(Args args) {
;     ...
;             if (nhalf > 0) { CONV_LD(0, va); CONV_LD(1, vb2);
;                 for (;;) { CONV_STEP(va, vc); if (s >= nhalf) break; CONV_STEP(vb2, va); if (s >= nhalf) break; CONV_STEP(vc, vb2); if (s >= nhalf) break; } }
.LBB0_571:
	s_cmp_ge_u32 s31, s12
	s_mov_b64 s[6:7], -1
	s_cbranch_scc1 .LBB0_543
	s_add_i32 s6, s34, 4
	s_min_i32 s6, s6, s13
	s_ashr_i32 s7, s6, 31
	s_lshr_b32 s7, s7, 30
	s_add_i32 s7, s6, s7
	s_lshr_b32 s8, s7, 2
	s_mul_i32 s8, s8, s99
	s_add_i32 s9, s8, s3
	s_mul_hi_i32 s8, s9, 0x2aaaaaab
	s_lshr_b32 s10, s8, 31
	s_ashr_i32 s8, s8, 7
	s_add_i32 s8, s8, s10
	s_mul_i32 s10, s8, 0x300
	s_and_b32 s7, s7, -4
	s_sub_i32 s36, s9, s10
	s_ashr_i32 s9, s8, 31
	s_sub_i32 s34, s6, s7
	s_cmpk_gt_i32 s36, 0x1ff
	s_mov_b64 s[6:7], -1
	s_cbranch_scc0 .LBB0_574
	v_readlane_b32 s40, v252, 16
	s_lshl_b64 s[6:7], s[8:9], 24
	v_readlane_b32 s52, v252, 28
	v_readlane_b32 s53, v252, 29
	s_add_u32 s6, s52, s6
	s_addc_u32 s7, s53, s7
	s_lshl_b32 s10, s36, 3
	s_and_b32 s10, s10, 0x700
	s_lshl_b32 s11, s34, 6
	s_add_i32 s37, s10, s11
	s_lshl_b32 s10, s36, 8
	s_and_b32 s10, s10, 0x1f00
	s_add_u32 s10, s6, s10
	v_readlane_b32 s41, v252, 17
	v_readlane_b32 s42, v252, 18
	v_readlane_b32 s43, v252, 19
	v_readlane_b32 s44, v252, 20
	v_readlane_b32 s45, v252, 21
	v_readlane_b32 s46, v252, 22
	v_readlane_b32 s47, v252, 23
	v_readlane_b32 s48, v252, 24
	v_readlane_b32 s49, v252, 25
	v_readlane_b32 s50, v252, 26
	v_readlane_b32 s51, v252, 27
	v_readlane_b32 s54, v252, 30
	v_readlane_b32 s55, v252, 31
	s_addc_u32 s11, s7, 0
	s_mov_b64 s[6:7], 0

; #define GAS __attribute__((address_space(1)))
; #define LAS __attribute__((address_space(3)))
; __device__ __forceinline__ unsigned pk4_fp8_nc(float a, float b, float c, float d) { int w = 0; w = __builtin_amdgcn_cvt_pk_fp8_f32(a, b, w, false); w = __builtin_amdgcn_cvt_pk_fp8_f32(c, d, w, true); return (unsigned)w; }
; __device__ __forceinline__ void tr_load2(const float* W, int N, int fl, int hh, int lane, f32x4 (&v)[16]) {
;     const int nblk = N / 64, kb = fl / nblk, nb = fl % nblk, k0 = 64 * NHB * kb + 64 * hh, n0 = 64 * nb;
;     const int g = lane >> 4, c4 = (lane & 15) * 4;
; #pragma unroll
;     for (int i = 0; i < 16; ++i) v[i] = *(const GAS f32x4*)(W + (size_t)(k0 + 16 * (i >> 2) + 4 * g + (i & 3)) * N + n0 + c4);
; }
; __device__ __forceinline__ void tr_half(const f32x4 (&v)[16], int hh, LAS unsigned* img, int lane, float scale) {
;     const int g = lane >> 4, m = lane & 15;
; #pragma unroll
;     for (int j = 0; j < 4; ++j) { const f32x4 a = v[4 * j] * scale, b = v[4 * j + 1] * scale, c = v[4 * j + 2] * scale, d = v[4 * j + 3] * scale;
;         const int dwi = (16 * hh + 4 * j + g) ^ ((m & 7) << 2);
;         img[(4 * m + 0) * (16 * NHB) + dwi] = pk4_fp8_nc(a.x, b.x, c.x, d.x); img[(4 * m + 1) * (16 * NHB) + dwi] = pk4_fp8_nc(a.y, b.y, c.y, d.y);
;         img[(4 * m + 2) * (16 * NHB) + dwi] = pk4_fp8_nc(a.z, b.z, c.z, d.z); img[(4 * m + 3) * (16 * NHB) + dwi] = pk4_fp8_nc(a.w, b.w, c.w, d.w); }
; }
.LBB0_576:
	v_or_b32_e32 v66, s37, v1
	v_mov_b32_e32 v211, v197
	v_ashrrev_i32_e32 v67, 31, v66
	v_lshl_add_u64 v[68:69], s[10:11], 0, v[210:211]
	v_lshlrev_b64 v[70:71], s6, v[66:67]
	v_lshl_add_u64 v[98:99], v[68:69], 0, v[70:71]
	v_or_b32_e32 v70, 1, v66
	v_ashrrev_i32_e32 v71, 31, v70
	v_lshlrev_b64 v[70:71], s6, v[70:71]
	v_lshl_add_u64 v[100:101], v[68:69], 0, v[70:71]
	v_or_b32_e32 v70, 2, v66
	v_ashrrev_i32_e32 v71, 31, v70
	v_lshlrev_b64 v[70:71], s6, v[70:71]
	v_lshl_add_u64 v[102:103], v[68:69], 0, v[70:71]
	v_or_b32_e32 v70, 3, v66
	v_ashrrev_i32_e32 v71, 31, v70
	v_lshlrev_b64 v[70:71], s6, v[70:71]
	v_lshl_add_u64 v[104:105], v[68:69], 0, v[70:71]
	v_or_b32_e32 v70, 16, v66
	v_ashrrev_i32_e32 v71, 31, v70
	v_lshlrev_b64 v[70:71], s6, v[70:71]
	v_lshl_add_u64 v[106:107], v[68:69], 0, v[70:71]
	v_or_b32_e32 v70, 17, v66
	v_ashrrev_i32_e32 v71, 31, v70
	v_lshlrev_b64 v[70:71], s6, v[70:71]
	v_lshl_add_u64 v[108:109], v[68:69], 0, v[70:71]
	v_or_b32_e32 v70, 18, v66
	v_ashrrev_i32_e32 v71, 31, v70
	v_lshlrev_b64 v[70:71], s6, v[70:71]
	v_lshl_add_u64 v[210:211], v[68:69], 0, v[70:71]
	v_or_b32_e32 v70, 19, v66
	v_ashrrev_i32_e32 v71, 31, v70
	v_lshlrev_b64 v[70:71], s6, v[70:71]
	v_lshl_add_u64 v[216:217], v[68:69], 0, v[70:71]
	v_or_b32_e32 v70, 32, v66
	v_ashrrev_i32_e32 v71, 31, v70
	v_lshlrev_b64 v[70:71], s6, v[70:71]
	v_lshl_add_u64 v[94:95], v[68:69], 0, v[70:71]
	v_or_b32_e32 v70, 33, v66
	v_ashrrev_i32_e32 v71, 31, v70
	v_lshlrev_b64 v[70:71], s6, v[70:71]
	v_lshl_add_u64 v[90:91], v[68:69], 0, v[70:71]
	v_or_b32_e32 v70, 34, v66
	v_ashrrev_i32_e32 v71, 31, v70
	v_lshlrev_b64 v[70:71], s6, v[70:71]
	v_lshl_add_u64 v[86:87], v[68:69], 0, v[70:71]
	v_or_b32_e32 v70, 35, v66
	v_ashrrev_i32_e32 v71, 31, v70
	v_lshlrev_b64 v[70:71], s6, v[70:71]
	v_lshl_add_u64 v[82:83], v[68:69], 0, v[70:71]
	v_or_b32_e32 v70, 48, v66
	v_ashrrev_i32_e32 v71, 31, v70
	v_lshlrev_b64 v[70:71], s6, v[70:71]
	v_lshl_add_u64 v[78:79], v[68:69], 0, v[70:71]
	v_or_b32_e32 v70, 49, v66
	v_ashrrev_i32_e32 v71, 31, v70
	v_lshlrev_b64 v[70:71], s6, v[70:71]
	v_lshl_add_u64 v[74:75], v[68:69], 0, v[70:71]
	v_or_b32_e32 v70, 50, v66
	v_or_b32_e32 v66, 51, v66
	v_ashrrev_i32_e32 v71, 31, v70
	v_ashrrev_i32_e32 v67, 31, v66
	v_lshlrev_b64 v[70:71], s6, v[70:71]
	v_lshlrev_b64 v[66:67], s6, v[66:67]
	v_lshl_add_u64 v[70:71], v[68:69], 0, v[70:71]
	v_lshl_add_u64 v[66:67], v[68:69], 0, v[66:67]
	global_load_dwordx4 v[66:69], v[66:67], off nt
	s_nop 0
	global_load_dwordx4 v[70:73], v[70:71], off nt
	s_nop 0
	global_load_dwordx4 v[74:77], v[74:75], off nt
	s_nop 0
	global_load_dwordx4 v[78:81], v[78:79], off nt
	s_nop 0
	global_load_dwordx4 v[82:85], v[82:83], off nt
	s_nop 0
	global_load_dwordx4 v[86:89], v[86:87], off nt
	s_nop 0
	global_load_dwordx4 v[90:93], v[90:91], off nt
	s_nop 0
	global_load_dwordx4 v[94:97], v[94:95], off nt
	s_nop 0
	global_load_dwordx4 v[126:129], v[98:99], off nt
	global_load_dwordx4 v[122:125], v[100:101], off nt
	global_load_dwordx4 v[118:121], v[102:103], off nt
	global_load_dwordx4 v[114:117], v[104:105], off nt
	global_load_dwordx4 v[110:113], v[106:107], off nt
	s_nop 0
	global_load_dwordx4 v[106:109], v[108:109], off nt
	s_nop 0
	global_load_dwordx4 v[98:101], v[216:217], off nt
	global_load_dwordx4 v[102:105], v[210:211], off nt
	v_pk_mul_f32 v[190:191], v[190:191], s[2:3] op_sel_hi:[1,0]
	v_pk_mul_f32 v[186:187], v[186:187], s[2:3] op_sel_hi:[1,0]
	v_mov_b32_e32 v211, v197
	v_cvt_pk_fp8_f32 v211, v190, v186
	v_mov_b32_e32 v186, v197
	v_pk_mul_f32 v[192:193], v[192:193], s[2:3] op_sel_hi:[1,0]
	v_pk_mul_f32 v[188:189], v[188:189], s[2:3] op_sel_hi:[1,0]
	v_cvt_pk_fp8_f32 v186, v191, v187
	v_mov_b32_e32 v187, v197
	v_cvt_pk_fp8_f32 v187, v192, v188
	v_mov_b32_e32 v188, v197
	v_cvt_pk_fp8_f32 v188, v193, v189
	v_pk_mul_f32 v[182:183], v[182:183], s[2:3] op_sel_hi:[1,0]
	v_pk_mul_f32 v[178:179], v[178:179], s[2:3] op_sel_hi:[1,0]
	s_and_b32 s6, s31, 3
	v_pk_mul_f32 v[184:185], v[184:185], s[2:3] op_sel_hi:[1,0]
	v_pk_mul_f32 v[180:181], v[180:181], s[2:3] op_sel_hi:[1,0]
	v_cvt_pk_fp8_f32 v211, v182, v178 op_sel:[0,0,1]
	v_cvt_pk_fp8_f32 v186, v183, v179 op_sel:[0,0,1]
	s_lshl_b32 s7, s6, 4
	v_cvt_pk_fp8_f32 v187, v184, v180 op_sel:[0,0,1]
	v_cvt_pk_fp8_f32 v188, v185, v181 op_sel:[0,0,1]
	v_bitop3_b32 v178, s7, v203, v201 bitop3:0x36
	v_lshl_add_u32 v178, v178, 2, v212
	ds_write2st64_b32 v178, v211, v186 offset1:1
; #define LAS __attribute__((address_space(3)))
; __device__ __forceinline__ unsigned pk4_fp8_nc(float a, float b, float c, float d) { int w = 0; w = __builtin_amdgcn_cvt_pk_fp8_f32(a, b, w, false); w = __builtin_amdgcn_cvt_pk_fp8_f32(c, d, w, true); return (unsigned)w; }
; __device__ __forceinline__ void tr_half(const f32x4 (&v)[16], int hh, LAS unsigned* img, int lane, float scale) {
;     const int g = lane >> 4, m = lane & 15;
; #pragma unroll
;     for (int j = 0; j < 4; ++j) { const f32x4 a = v[4 * j] * scale, b = v[4 * j + 1] * scale, c = v[4 * j + 2] * scale, d = v[4 * j + 3] * scale;
;         const int dwi = (16 * hh + 4 * j + g) ^ ((m & 7) << 2);
;         img[(4 * m + 0) * (16 * NHB) + dwi] = pk4_fp8_nc(a.x, b.x, c.x, d.x); img[(4 * m + 1) * (16 * NHB) + dwi] = pk4_fp8_nc(a.y, b.y, c.y, d.y);
;         img[(4 * m + 2) * (16 * NHB) + dwi] = pk4_fp8_nc(a.z, b.z, c.z, d.z); img[(4 * m + 3) * (16 * NHB) + dwi] = pk4_fp8_nc(a.w, b.w, c.w, d.w); }
; }
	ds_write2st64_b32 v178, v187, v188 offset0:2 offset1:3
	v_pk_mul_f32 v[174:175], v[174:175], s[2:3] op_sel_hi:[1,0]
	v_pk_mul_f32 v[170:171], v[170:171], s[2:3] op_sel_hi:[1,0]
	v_mov_b32_e32 v178, v197
	v_cvt_pk_fp8_f32 v178, v174, v170
	v_mov_b32_e32 v170, v197
	v_pk_mul_f32 v[176:177], v[176:177], s[2:3] op_sel_hi:[1,0]
	v_pk_mul_f32 v[172:173], v[172:173], s[2:3] op_sel_hi:[1,0]
	v_cvt_pk_fp8_f32 v170, v175, v171
	v_mov_b32_e32 v171, v197
	v_cvt_pk_fp8_f32 v171, v176, v172
	v_mov_b32_e32 v172, v197
	v_cvt_pk_fp8_f32 v172, v177, v173
	v_pk_mul_f32 v[166:167], v[166:167], s[2:3] op_sel_hi:[1,0]
	v_pk_mul_f32 v[162:163], v[162:163], s[2:3] op_sel_hi:[1,0]
	v_pk_mul_f32 v[168:169], v[168:169], s[2:3] op_sel_hi:[1,0]
	v_pk_mul_f32 v[164:165], v[164:165], s[2:3] op_sel_hi:[1,0]
	v_cvt_pk_fp8_f32 v178, v166, v162 op_sel:[0,0,1]
	v_cvt_pk_fp8_f32 v170, v167, v163 op_sel:[0,0,1]
	v_or_b32_e32 v210, s7, v201
	v_cvt_pk_fp8_f32 v171, v168, v164 op_sel:[0,0,1]
	v_cvt_pk_fp8_f32 v172, v169, v165 op_sel:[0,0,1]
	v_bitop3_b32 v162, v210, v203, 4 bitop3:0x36
	v_lshl_add_u32 v162, v162, 2, v212
	ds_write2st64_b32 v162, v178, v170 offset1:1
	ds_write2st64_b32 v162, v171, v172 offset0:2 offset1:3
	v_pk_mul_f32 v[158:159], v[158:159], s[2:3] op_sel_hi:[1,0]
	v_pk_mul_f32 v[154:155], v[154:155], s[2:3] op_sel_hi:[1,0]
	v_mov_b32_e32 v162, v197
	v_cvt_pk_fp8_f32 v162, v158, v154
	v_mov_b32_e32 v154, v197
	v_cvt_pk_fp8_f32 v154, v159, v155
	v_pk_mul_f32 v[150:151], v[150:151], s[2:3] op_sel_hi:[1,0]
	v_pk_mul_f32 v[146:147], v[146:147], s[2:3] op_sel_hi:[1,0]
	v_pk_mul_f32 v[142:143], v[142:143], s[2:3] op_sel_hi:[1,0]
	v_cvt_pk_fp8_f32 v154, v151, v147 op_sel:[0,0,1]
	v_pk_mul_f32 v[138:139], v[138:139], s[2:3] op_sel_hi:[1,0]
	v_mov_b32_e32 v147, v197
	v_pk_mul_f32 v[160:161], v[160:161], s[2:3] op_sel_hi:[1,0]
	v_pk_mul_f32 v[156:157], v[156:157], s[2:3] op_sel_hi:[1,0]
	v_mov_b32_e32 v155, v197
	v_cvt_pk_fp8_f32 v147, v142, v138
	v_mov_b32_e32 v138, v197
	v_cvt_pk_fp8_f32 v155, v160, v156
	v_mov_b32_e32 v156, v197
	v_pk_mul_f32 v[144:145], v[144:145], s[2:3] op_sel_hi:[1,0]
	v_pk_mul_f32 v[140:141], v[140:141], s[2:3] op_sel_hi:[1,0]
	v_cvt_pk_fp8_f32 v138, v143, v139
	v_mov_b32_e32 v139, v197
	v_cvt_pk_fp8_f32 v156, v161, v157
	v_cvt_pk_fp8_f32 v139, v144, v140
	v_mov_b32_e32 v140, v197
	v_cvt_pk_fp8_f32 v140, v145, v141
	v_pk_mul_f32 v[152:153], v[152:153], s[2:3] op_sel_hi:[1,0]
	v_pk_mul_f32 v[148:149], v[148:149], s[2:3] op_sel_hi:[1,0]
	v_cvt_pk_fp8_f32 v162, v150, v146 op_sel:[0,0,1]
	v_cvt_pk_fp8_f32 v155, v152, v148 op_sel:[0,0,1]
	v_cvt_pk_fp8_f32 v156, v153, v149 op_sel:[0,0,1]
	v_pk_mul_f32 v[136:137], v[136:137], s[2:3] op_sel_hi:[1,0]
	v_pk_mul_f32 v[134:135], v[134:135], s[2:3] op_sel_hi:[1,0]
	v_pk_mul_f32 v[132:133], v[132:133], s[2:3] op_sel_hi:[1,0]
	v_pk_mul_f32 v[130:131], v[130:131], s[2:3] op_sel_hi:[1,0]
	v_bitop3_b32 v146, v210, v203, 8 bitop3:0x36
	v_cvt_pk_fp8_f32 v147, v134, v130 op_sel:[0,0,1]
	v_cvt_pk_fp8_f32 v138, v135, v131 op_sel:[0,0,1]
	v_cvt_pk_fp8_f32 v139, v136, v132 op_sel:[0,0,1]
	v_cvt_pk_fp8_f32 v140, v137, v133 op_sel:[0,0,1]
	v_lshl_add_u32 v146, v146, 2, v212
	ds_write2st64_b32 v146, v162, v154 offset1:1
	ds_write2st64_b32 v146, v155, v156 offset0:2 offset1:3
	v_bitop3_b32 v146, v210, v203, 12 bitop3:0x36
	v_lshl_add_u32 v130, v146, 2, v212
	s_cmp_lg_u32 s6, 3
	ds_write2st64_b32 v130, v147, v138 offset1:1
	ds_write2st64_b32 v130, v139, v140 offset0:2 offset1:3
	s_cbranch_scc1 .LBB0_542
	s_lshr_b32 s6, s31, 2
	s_mul_i32 s6, s6, s99
	s_add_i32 s7, s6, s3
	s_mul_hi_i32 s6, s7, 0x2aaaaaab
	s_lshr_b32 s8, s6, 31
	s_ashr_i32 s6, s6, 7
	s_add_i32 s6, s6, s8
	s_mul_i32 s8, s6, 0x300
	s_sub_i32 s10, s7, s8
	s_ashr_i32 s7, s6, 31
	s_cmpk_gt_i32 s10, 0x1ff
	s_mov_b64 s[8:9], -1
	s_cbranch_scc0 .LBB0_581
	s_and_b32 s31, s10, 31
	s_lshl_b32 s9, s10, 3
	s_lshl_b64 s[38:39], s[6:7], 22
	s_lshl_b32 s31, s31, 17
	s_lshl_b64 s[36:37], s[6:7], 11
	s_and_b32 s9, s9, 0x700
	s_lshl_b32 s11, s10, 6
	s_or_b32 s31, s38, s31
	s_and_b32 s11, s11, 0x7c0
	s_waitcnt lgkmcnt(0)
	s_or_b32 s38, s31, s9
	v_or_b32_e32 v132, s36, v202
	v_mov_b32_e32 v133, s37
	v_or_b32_e32 v132, s11, v132
	s_add_u32 s36, s29, s9
	v_lshlrev_b64 v[132:133], 11, v[132:133]
	s_addc_u32 s37, s72, 0
	s_mov_b32 s8, 3
	v_lshl_add_u64 v[130:131], v[204:205], 0, s[38:39]
	v_lshl_add_u64 v[132:133], s[36:37], 0, v[132:133]
	v_mov_b32_e32 v134, v214

; #define LAS __attribute__((address_space(3)))
; __global__ void __launch_bounds__(NTHR, 2) mk_fwd(Args args) {
;     ...
;         const int xcd_i = bx % 8, slot_i = bx / 8;
;         constexpr int NSCAN_X = 8;
;         if (slot_i < NSCAN_X) {
;             constexpr int CH = 16, NCHUNK = SEQ / CH, NSLOT = 8, LAG = 3;
;             LAS unsigned* ring_ready = (LAS unsigned*)(lds + LDSCTL_OFF + 896); LAS unsigned* ring_done = ring_ready + 4;
;             constexpr int PK_PA = 0, PK_PR = 2048, PK_QQ = 4096, PK_TT = 5120, PK_GG = 6144, PK_BK = 7168, PK_VT = 11264, PK_WC = 13312, PK_BON = 13568, PK_BYTES = 16384;
;             const int hd = xcd_i * NSCAN_X + slot_i, b = hd >> 4, h = hd & 15;
;             const size_t mbase = (size_t)b * SEQ;
;             static_assert((size_t)64 * NCHUNK * PK_BYTES <= 4 * SZ_F1K, "packs fit the four unused f32 [M][1024] buffers at WS_R");
;             unsigned char* PACK = ws + WS_R + (size_t)hd * NCHUNK * PK_BYTES;
;             const int tr = lane & 15, q = lane >> 4;
;             if (wave < 4) {
;     ...
;             } else {
;                 const int lw = wave - 4;
.LBB0_585:
	s_cmp_lg_u32 s98, 0
	s_cbranch_scc1 .Lconv_p1_return
	s_mov_b64 s[2:3], 0
.LBB0_586:
	s_andn2_b64 vcc, exec, s[2:3]
	s_cbranch_vccnz .LBB0_670
	v_readlane_b32 s2, v252, 38
	s_lshl_b32 s2, s2, 3
	v_readlane_b32 s3, v252, 39
	s_add_i32 s6, s2, s3
	v_readlane_b32 s10, v252, 42
	s_cmpk_gt_u32 s10, 0xff
	s_mov_b64 s[2:3], -1
	s_cbranch_scc0 .LBB0_611
	v_writelane_b32 v252, s0, 54
	v_writelane_b32 v252, s1, 55
	v_writelane_b32 v252, s28, 56
	v_writelane_b32 v252, s29, 57
	v_writelane_b32 v252, s30, 58
	v_writelane_b32 v252, s72, 59
	v_writelane_b32 v252, s86, 60
	v_writelane_b32 v252, s90, 61
	v_writelane_b32 v252, s91, 62
	v_readlane_b32 s4, v252, 43
	s_nop 3
	s_sub_i32 s4, s4, 4
	s_lshr_b32 s5, s6, 4
	s_and_b32 s7, s6, 15
	s_lshl_b32 s5, s5, 12
	s_or_b32 s5, s5, s7
	s_lshl_b32 s7, s4, 4
	s_or_b32 s30, s5, s7
	s_movk_i32 s28, 64
	s_add_u32 s10, s26, 0x6008000
	s_addc_u32 s11, s27, 0
	s_and_b32 s101, s30, 0xfffff000
	s_add_i32 s101, s101, 2176
	s_lshl_b32 s100, s4, 14
	s_lshl_b32 s98, s4, 2
	s_add_i32 s98, s98, 0x27380
	v_mov_b32_e32 v1, s98
	v_mov_b32_e32 v2, s4
	ds_write_b32 v1, v2
	s_waitcnt vmcnt(0) lgkmcnt(0)
	s_branch .Lprod_code

; #define LAS __attribute__((address_space(3)))
; __global__ void __launch_bounds__(NTHR, 2) mk_fwd(Args args) {
;     ...
;                 for (int c = 0; c < NCHUNK + LAG; ++c) {
;                     if (c < NCHUNK) {
;                         if (c >= NSLOT) { const unsigned want = (unsigned)(c - NSLOT + 1); unsigned sp_ = 0;
;                             for (;;) { const v4u dd_ = *(volatile LAS v4u*)ring_done; if (min(min(dd_.x, dd_.y), min(dd_.z, dd_.w)) >= want) break; __builtin_amdgcn_s_sleep(0); if (++sp_ > (1u << 26)) break; } }
;                         asm volatile("" ::: "memory");
;                         const unsigned char* src = PACK + (size_t)c * PK_BYTES + lw * 1024 + lane * 16;
;                         LAS unsigned char* dst = lds + (c & (NSLOT - 1)) * PK_BYTES + lw * 1024;
; #pragma unroll
;                         for (int p = 0; p < 3; ++p) __builtin_amdgcn_global_load_lds((const unsigned*)(src + p * 4096), (LAS unsigned*)(dst + p * 4096), 16, 0, 0);
.Lld_gok:
	buffer_inv sc1
	s_waitcnt vmcnt(0)
	s_movk_i32 s39, 136
	s_mov_b32 s9, 0

; #define LAS __attribute__((address_space(3)))
; __global__ void __launch_bounds__(NTHR, 2) mk_fwd(Args args) {
;     ...
;                         const unsigned char* src = PACK + (size_t)c * PK_BYTES + lw * 1024 + lane * 16;
;                         LAS unsigned char* dst = lds + (c & (NSLOT - 1)) * PK_BYTES + lw * 1024;
; #pragma unroll
;                         for (int p = 0; p < 3; ++p) __builtin_amdgcn_global_load_lds((const unsigned*)(src + p * 4096), (LAS unsigned*)(dst + p * 4096), 16, 0, 0);
;                         if (lw < 2) __builtin_amdgcn_global_load_lds((const unsigned*)(src + 3 * 4096), (LAS unsigned*)(dst + 3 * 4096), 16, 0, 0);
;                     }
;                     if (c >= LAG) {
;                         if (c < NCHUNK) { if (lw < 2) asm volatile("s_waitcnt vmcnt(12)" ::: "memory"); else asm volatile("s_waitcnt vmcnt(9)" ::: "memory"); } else asm volatile("s_waitcnt vmcnt(0)" ::: "memory");
;                         if (lane == 0) __hip_atomic_fetch_add(ring_ready + lw, 1u, __ATOMIC_RELAXED, __HIP_MEMORY_SCOPE_WORKGROUP);
;                     }
.Lld_sok:
	s_lshl_b32 s8, s39, 14
	v_lshl_add_u64 v[4:5], v[2:3], 0, s[8:9]
	s_and_b32 s8, s8, 0xc000
	s_add_i32 s8, s8, s7
	s_mov_b32 m0, s8
	v_lshl_add_u64 v[6:7], v[4:5], 0, s[12:13]
	global_load_lds_dwordx4 v[4:5], off
	s_add_i32 m0, s8, 0x1000
	s_nop 0
	global_load_lds_dwordx4 v[6:7], off
	v_lshl_add_u64 v[6:7], v[4:5], 0, s[14:15]
	s_add_i32 m0, s8, 0x2000
	s_nop 0
	global_load_lds_dwordx4 v[6:7], off
	s_cmpk_gt_u32 s7, 0x400
	s_cbranch_scc1 .Lld_three
	v_lshl_add_u64 v[6:7], v[4:5], 0, s[16:17]
	s_add_i32 m0, s8, 0x3000
	s_nop 0
	global_load_lds_dwordx4 v[6:7], off
	s_cmpk_eq_i32 s39, 136
	s_cbranch_scc1 .Lld_next
	s_waitcnt vmcnt(4)
	s_branch .Lld_pub
.Lld_three:
	s_cmpk_eq_i32 s39, 136
	s_cbranch_scc1 .Lld_next
	s_waitcnt vmcnt(3)
